# nt hint also on the conv phase's output stores (P2)
# baseline (speedup 1.0000x reference)
.LBB0_264:
	s_or_b64 exec, exec, s[6:7]
	s_waitcnt vmcnt(0)
	v_lshlrev_b32_e32 v136, 16, v126
	v_and_b32_e32 v126, 0xffff0000, v126
	v_fma_f32 v137, v19, v126, v31
	v_lshlrev_b32_e32 v126, 16, v127
	v_fma_f32 v138, v20, v126, v32
	v_and_b32_e32 v126, 0xffff0000, v127
	v_fma_f32 v139, v21, v126, v33
	v_lshlrev_b32_e32 v126, 16, v128
	v_fma_f32 v142, v14, v126, v26
	v_and_b32_e32 v126, 0xffff0000, v128
	v_fma_f32 v143, v15, v126, v27
	v_lshlrev_b32_e32 v126, 16, v129
	v_fma_f32 v144, v16, v126, v28
	v_and_b32_e32 v126, 0xffff0000, v129
	v_fma_f32 v145, v17, v126, v29
	v_lshlrev_b32_e32 v141, 16, v122
	v_lshlrev_b32_e32 v140, 16, v114
	v_mov_b32_e32 v126, v106
	v_mov_b32_e32 v127, v22
	v_fma_f32 v136, v18, v136, v30
	v_pk_mul_f32 v[128:129], v[126:127], v[140:141]
	v_and_b32_e32 v147, 0xffff0000, v122
	v_add_f32_e32 v22, v136, v128
	v_add_f32_e32 v136, v22, v129
	v_and_b32_e32 v146, 0xffff0000, v114
	v_mov_b32_e32 v22, v107
	v_pk_mul_f32 v[106:107], v[22:23], v[146:147]
	v_lshlrev_b32_e32 v150, 16, v115
	v_add_f32_e32 v106, v137, v106
	v_add_f32_e32 v137, v106, v107
	v_lshlrev_b32_e32 v151, 16, v123
	v_mov_b32_e32 v106, v108
	v_mov_b32_e32 v107, v24
	v_pk_mul_f32 v[128:129], v[106:107], v[150:151]
	v_and_b32_e32 v123, 0xffff0000, v123
	v_add_f32_e32 v24, v138, v128
	v_add_f32_e32 v138, v24, v129
	v_and_b32_e32 v122, 0xffff0000, v115
	v_mov_b32_e32 v24, v109
	v_pk_mul_f32 v[108:109], v[24:25], v[122:123]
	v_lshlrev_b32_e32 v153, 16, v124
	v_add_f32_e32 v108, v139, v108
	v_add_f32_e32 v148, v108, v109
	v_lshlrev_b32_e32 v152, 16, v116
	v_mov_b32_e32 v108, v102
	v_mov_b32_e32 v109, v10
	v_pk_mul_f32 v[114:115], v[108:109], v[152:153]
	v_and_b32_e32 v155, 0xffff0000, v124
	v_add_f32_e32 v10, v142, v114
	v_add_f32_e32 v149, v10, v115
	v_and_b32_e32 v154, 0xffff0000, v116
	v_mov_b32_e32 v10, v103
	v_pk_mul_f32 v[102:103], v[10:11], v[154:155]
	v_lshlrev_b32_e32 v156, 16, v117
	v_add_f32_e32 v102, v143, v102
	v_add_f32_e32 v116, v102, v103
	v_lshlrev_b32_e32 v157, 16, v125
	v_mov_b32_e32 v102, v104
	v_mov_b32_e32 v103, v12
	v_pk_mul_f32 v[114:115], v[102:103], v[156:157]
	v_and_b32_e32 v159, 0xffff0000, v125
	v_add_f32_e32 v12, v144, v114
	v_add_f32_e32 v160, v12, v115
	v_and_b32_e32 v158, 0xffff0000, v117
	v_mov_b32_e32 v12, v105
	v_pk_mul_f32 v[104:105], v[12:13], v[158:159]
	v_lshlrev_b32_e32 v125, 16, v118
	v_add_f32_e32 v104, v145, v104
	v_add_f32_e32 v117, v104, v105
	v_lshlrev_b32_e32 v124, 16, v110
	v_mov_b32_e32 v104, v98
	v_mov_b32_e32 v105, v6
	v_pk_mul_f32 v[114:115], v[104:105], v[124:125]
	v_and_b32_e32 v129, 0xffff0000, v118
	v_add_f32_e32 v6, v136, v114
	v_add_f32_e32 v161, v6, v115
	v_and_b32_e32 v128, 0xffff0000, v110
	v_mov_b32_e32 v6, v99
	v_pk_mul_f32 v[98:99], v[6:7], v[128:129]
	v_lshlrev_b32_e32 v136, 16, v111
	v_add_f32_e32 v98, v137, v98
	v_add_f32_e32 v118, v98, v99
	v_lshlrev_b32_e32 v137, 16, v119
	v_mov_b32_e32 v98, v100
	v_mov_b32_e32 v99, v8
	v_pk_mul_f32 v[114:115], v[98:99], v[136:137]
	v_and_b32_e32 v139, 0xffff0000, v119
	v_add_f32_e32 v8, v138, v114
	v_add_f32_e32 v114, v8, v115
	v_and_b32_e32 v138, 0xffff0000, v111
	v_mov_b32_e32 v8, v101
	v_pk_mul_f32 v[100:101], v[8:9], v[138:139]
	v_lshlrev_b32_e32 v143, 16, v120
	v_add_f32_e32 v100, v148, v100
	v_add_f32_e32 v115, v100, v101
	v_lshlrev_b32_e32 v142, 16, v112
	v_mov_b32_e32 v100, v94
	v_mov_b32_e32 v101, v2
	v_pk_mul_f32 v[110:111], v[100:101], v[142:143]
	v_and_b32_e32 v145, 0xffff0000, v120
	v_add_f32_e32 v2, v149, v110
	v_add_f32_e32 v119, v2, v111
	v_and_b32_e32 v144, 0xffff0000, v112
	v_mov_b32_e32 v2, v95
	v_pk_mul_f32 v[94:95], v[2:3], v[144:145]
	v_lshlrev_b32_e32 v148, 16, v113
	v_add_f32_e32 v94, v116, v94
	v_add_f32_e32 v112, v94, v95
	v_lshlrev_b32_e32 v149, 16, v121
	v_mov_b32_e32 v94, v96
	v_mov_b32_e32 v95, v4
	v_pk_mul_f32 v[110:111], v[94:95], v[148:149]
	v_mul_f32_e32 v96, 0xbfb8aa3b, v161
	v_add_f32_e32 v4, v160, v110
	v_add_f32_e32 v110, v4, v111
	v_and_b32_e32 v120, 0xffff0000, v113
	v_exp_f32_e32 v111, v96
	v_mul_f32_e32 v113, 0xbfb8aa3b, v114
	v_and_b32_e32 v121, 0xffff0000, v121
	v_mov_b32_e32 v4, v97
	v_exp_f32_e32 v113, v113
	v_pk_mul_f32 v[96:97], v[4:5], v[120:121]
	v_mul_f32_e32 v116, 0xbfb8aa3b, v115
	v_add_f32_e32 v96, v117, v96
	v_add_f32_e32 v96, v96, v97
	v_add_f32_e32 v97, 1.0, v111
	v_mul_f32_e32 v111, 0xbfb8aa3b, v118
	v_exp_f32_e32 v111, v111
	v_add_f32_e32 v113, 1.0, v113
	v_rcp_f32_e32 v113, v113
	v_exp_f32_e32 v116, v116
	v_add_f32_e32 v111, 1.0, v111
	v_rcp_f32_e32 v111, v111
	v_mul_f32_e32 v113, v114, v113
	v_add_f32_e32 v114, 1.0, v116
	v_mul_f32_e32 v116, 0xbfb8aa3b, v119
	v_mul_f32_e32 v117, 0xbfb8aa3b, v112
	v_rcp_f32_e32 v114, v114
	v_exp_f32_e32 v116, v116
	v_exp_f32_e32 v117, v117
	v_mul_f32_e32 v111, v118, v111
	v_mul_f32_e32 v118, 0xbfb8aa3b, v96
	v_mul_f32_e32 v114, v115, v114
	v_add_f32_e32 v115, 1.0, v116
	v_add_f32_e32 v116, 1.0, v117
	v_mul_f32_e32 v117, 0xbfb8aa3b, v110
	v_exp_f32_e32 v118, v118
	v_exp_f32_e32 v117, v117
	v_rcp_f32_e32 v97, v97
	v_rcp_f32_e32 v115, v115
	v_add_f32_e32 v118, 1.0, v118
	v_add_f32_e32 v117, 1.0, v117
	v_rcp_f32_e32 v118, v118
	v_rcp_f32_e32 v116, v116
	v_rcp_f32_e32 v117, v117
	v_mul_f32_e32 v97, v161, v97
	v_mul_f32_e32 v115, v119, v115
	v_mul_f32_e32 v96, v96, v118
	v_mul_f32_e32 v116, v112, v116
	v_mul_f32_e32 v110, v110, v117
	v_cvt_pk_bf16_f32 v112, v97, v111
	v_cvt_pk_bf16_f32 v113, v113, v114
	v_cvt_pk_bf16_f32 v114, v115, v116
	v_cvt_pk_bf16_f32 v115, v110, v96
	v_mov_b64_e32 v[96:97], s[12:13]
	v_mad_i64_i32 v[116:117], s[6:7], v131, s35, v[96:97]
	v_lshlrev_b64 v[110:111], 1, v[134:135]
	v_lshl_add_u64 v[116:117], v[116:117], 0, v[110:111]
	global_store_dwordx4 v[116:117], v[112:115], off nt
	v_fma_f32 v116, v20, v150, v32
	v_fma_f32 v134, v16, v156, v28
	v_pk_mov_b32 v[112:113], v[140:141], v[124:125] op_sel:[1,0]
	v_fma_f32 v114, v18, v140, v30
	v_pk_mul_f32 v[112:113], v[126:127], v[112:113]
	v_fma_f32 v115, v19, v146, v31
	v_add_f32_e32 v112, v114, v112
	v_add_f32_e32 v140, v112, v113
	v_pk_mov_b32 v[112:113], v[146:147], v[128:129] op_sel:[1,0]
	v_fma_f32 v117, v21, v122, v33
	v_pk_mul_f32 v[112:113], v[22:23], v[112:113]
	v_fma_f32 v118, v14, v152, v26
	v_add_f32_e32 v112, v115, v112
	v_add_f32_e32 v146, v112, v113
	v_pk_mov_b32 v[112:113], v[150:151], v[136:137] op_sel:[1,0]
	v_fma_f32 v119, v15, v154, v27
	v_pk_mul_f32 v[112:113], v[106:107], v[112:113]
	v_fma_f32 v135, v17, v158, v29
	v_add_f32_e32 v112, v116, v112
	v_add_f32_e32 v156, v112, v113
	v_pk_mov_b32 v[112:113], v[122:123], v[138:139] op_sel:[1,0]
	v_fma_f32 v114, v18, v141, v30
	v_pk_mul_f32 v[112:113], v[24:25], v[112:113]
	v_fma_f32 v115, v19, v147, v31
	v_add_f32_e32 v112, v117, v112
	v_add_f32_e32 v162, v112, v113
	v_pk_mov_b32 v[112:113], v[152:153], v[142:143] op_sel:[1,0]
	v_fma_f32 v116, v20, v151, v32
	v_pk_mul_f32 v[112:113], v[108:109], v[112:113]
	v_fma_f32 v117, v21, v123, v33
	v_add_f32_e32 v112, v118, v112
	v_add_f32_e32 v163, v112, v113
	v_pk_mov_b32 v[112:113], v[154:155], v[144:145] op_sel:[1,0]
	v_fma_f32 v118, v14, v153, v26
	v_pk_mul_f32 v[112:113], v[10:11], v[112:113]
	v_fma_f32 v122, v16, v157, v28
	v_add_f32_e32 v112, v119, v112
	v_add_f32_e32 v164, v112, v113
	v_pk_mov_b32 v[112:113], v[156:157], v[148:149] op_sel:[1,0]
	v_fma_f32 v119, v15, v155, v27
	v_pk_mul_f32 v[112:113], v[102:103], v[112:113]
	v_fma_f32 v123, v17, v159, v29
	v_add_f32_e32 v112, v134, v112
	v_add_f32_e32 v165, v112, v113
	v_pk_mov_b32 v[112:113], v[158:159], v[120:121] op_sel:[1,0]
	v_add_u32_e32 v1, s0, v1
	v_pk_mul_f32 v[112:113], v[12:13], v[112:113]
	v_cmp_lt_i32_e32 vcc, s36, v1
	v_add_f32_e32 v112, v135, v112
	v_add_f32_e32 v166, v112, v113
	v_or_b32_e32 v112, 1, v131
	v_mad_i64_i32 v[112:113], s[6:7], v112, s35, v[96:97]
	v_lshl_add_u64 v[160:161], v[112:113], 0, v[110:111]
	v_pk_mul_f32 v[112:113], v[126:127], v[124:125]
	s_or_b64 s[16:17], vcc, s[16:17]
	v_add_f32_e32 v112, v114, v112
	v_add_f32_e32 v134, v112, v113
	v_pk_mul_f32 v[112:113], v[22:23], v[128:129]
	v_add_u32_e32 v130, s1, v130
	v_add_f32_e32 v112, v115, v112
	v_add_f32_e32 v135, v112, v113
	v_pk_mul_f32 v[112:113], v[106:107], v[136:137]
	v_pk_mul_f32 v[114:115], v[102:103], v[148:149]
	v_add_f32_e32 v112, v116, v112
	v_add_f32_e32 v141, v112, v113
	v_pk_mul_f32 v[112:113], v[24:25], v[138:139]
	v_add_f32_e32 v114, v122, v114
	v_add_f32_e32 v112, v117, v112
	v_add_f32_e32 v147, v112, v113
	v_pk_mul_f32 v[112:113], v[108:109], v[142:143]
	v_add_f32_e32 v169, v114, v115
	v_add_f32_e32 v112, v118, v112
	v_add_f32_e32 v167, v112, v113
	v_pk_mul_f32 v[112:113], v[10:11], v[144:145]
	v_and_b32_e32 v115, 0xffff0000, v90
	v_add_f32_e32 v112, v119, v112
	v_add_f32_e32 v168, v112, v113
	v_lshlrev_b32_e32 v113, 16, v90
	v_lshlrev_b32_e32 v112, 16, v86
	v_pk_mov_b32 v[150:151], v[124:125], v[112:113] op_sel:[1,0]
	s_nop 0
	v_pk_mul_f32 v[116:117], v[104:105], v[150:151]
	s_nop 0
	v_add_f32_e32 v116, v140, v116
	v_add_f32_e32 v140, v116, v117
	v_mul_f32_e32 v116, 0xbfb8aa3b, v140
	v_exp_f32_e32 v118, v116
	v_pk_mul_f32 v[116:117], v[12:13], v[120:121]
	v_add_f32_e32 v114, 1.0, v118
	v_rcp_f32_e32 v122, v114
	v_and_b32_e32 v114, 0xffff0000, v86
	v_pk_mov_b32 v[152:153], v[128:129], v[114:115] op_sel:[1,0]
	v_add_f32_e32 v116, v123, v116
	v_pk_mul_f32 v[118:119], v[6:7], v[152:153]
	v_add_f32_e32 v170, v116, v117
	v_add_f32_e32 v86, v146, v118
	v_add_f32_e32 v86, v86, v119
	v_mul_f32_e32 v90, 0xbfb8aa3b, v86
	v_exp_f32_e32 v90, v90
	v_pk_mul_f32 v[116:117], v[104:105], v[112:113]
	v_mul_f32_e32 v140, v140, v122
	v_add_f32_e32 v116, v134, v116
	v_add_f32_e32 v90, 1.0, v90
	v_rcp_f32_e32 v90, v90
	v_add_f32_e32 v171, v116, v117
	v_lshlrev_b32_e32 v116, 16, v87
	v_lshlrev_b32_e32 v117, 16, v91
	v_pk_mov_b32 v[154:155], v[136:137], v[116:117] op_sel:[1,0]
	v_mul_f32_e32 v86, v86, v90
	v_pk_mul_f32 v[122:123], v[98:99], v[154:155]
	v_pk_mul_f32 v[118:119], v[6:7], v[114:115]
	v_add_f32_e32 v90, v156, v122
	v_add_f32_e32 v134, v90, v123
	v_mul_f32_e32 v90, 0xbfb8aa3b, v134
	v_exp_f32_e32 v90, v90
	v_add_f32_e32 v118, v135, v118
	v_add_f32_e32 v172, v118, v119
	v_and_b32_e32 v119, 0xffff0000, v91
	v_add_f32_e32 v90, 1.0, v90
	v_and_b32_e32 v118, 0xffff0000, v87
	v_rcp_f32_e32 v135, v90
	v_pk_mov_b32 v[90:91], v[138:139], v[118:119] op_sel:[1,0]
	v_cvt_pk_bf16_f32 v86, v140, v86
	v_mul_f32_e32 v146, v134, v135
	v_pk_mul_f32 v[122:123], v[8:9], v[90:91]
	v_pk_mul_f32 v[134:135], v[98:99], v[116:117]
	v_add_f32_e32 v87, v162, v122
	v_add_f32_e32 v87, v87, v123
	v_mul_f32_e32 v122, 0xbfb8aa3b, v87
	v_exp_f32_e32 v122, v122
	v_lshlrev_b32_e32 v123, 16, v92
	v_add_f32_e32 v134, v141, v134
	v_add_f32_e32 v173, v134, v135
	v_add_f32_e32 v122, 1.0, v122
	v_rcp_f32_e32 v158, v122
	v_lshlrev_b32_e32 v122, 16, v88
	v_pk_mov_b32 v[156:157], v[142:143], v[122:123] op_sel:[1,0]
	v_pk_mul_f32 v[134:135], v[8:9], v[118:119]
	v_pk_mul_f32 v[140:141], v[100:101], v[156:157]
	v_add_f32_e32 v134, v147, v134
	v_add_f32_e32 v140, v163, v140
	v_add_f32_e32 v140, v140, v141
	v_mul_f32_e32 v141, 0xbfb8aa3b, v140
	v_exp_f32_e32 v141, v141
	v_add_f32_e32 v174, v134, v135
	v_and_b32_e32 v135, 0xffff0000, v92
	v_and_b32_e32 v134, 0xffff0000, v88
	v_add_f32_e32 v141, 1.0, v141
	v_rcp_f32_e32 v141, v141
	v_mul_f32_e32 v87, v87, v158
	v_pk_mov_b32 v[158:159], v[144:145], v[134:135] op_sel:[1,0]
	v_cvt_pk_bf16_f32 v87, v146, v87
	v_mul_f32_e32 v175, v140, v141
	v_pk_mul_f32 v[140:141], v[2:3], v[158:159]
	s_nop 0
	v_add_f32_e32 v88, v164, v140
	v_add_f32_e32 v88, v88, v141
	v_pk_mul_f32 v[140:141], v[100:101], v[122:123]
	v_mul_f32_e32 v92, 0xbfb8aa3b, v88
	v_add_f32_e32 v140, v167, v140
	v_add_f32_e32 v167, v140, v141
	v_lshlrev_b32_e32 v140, 16, v89
	v_lshlrev_b32_e32 v141, 16, v93
	v_exp_f32_e32 v92, v92
	v_pk_mov_b32 v[162:163], v[148:149], v[140:141] op_sel:[1,0]
	v_add_f32_e32 v92, 1.0, v92
	v_pk_mul_f32 v[146:147], v[94:95], v[162:163]
	v_rcp_f32_e32 v92, v92
	v_add_f32_e32 v146, v165, v146
	v_add_f32_e32 v176, v146, v147
	v_mul_f32_e32 v146, 0xbfb8aa3b, v176
	v_exp_f32_e32 v146, v146
	v_mul_f32_e32 v177, v88, v92
	v_and_b32_e32 v147, 0xffff0000, v93
	v_pk_mul_f32 v[164:165], v[2:3], v[134:135]
	v_add_f32_e32 v88, 1.0, v146
	v_and_b32_e32 v146, 0xffff0000, v89
	v_pk_mov_b32 v[92:93], v[120:121], v[146:147] op_sel:[1,0]
	v_add_f32_e32 v164, v168, v164
	v_rcp_f32_e32 v168, v88
	v_pk_mul_f32 v[88:89], v[4:5], v[92:93]
	v_fma_f32 v120, v17, v120, v29
	v_add_f32_e32 v88, v166, v88
	v_add_f32_e32 v89, v88, v89
	v_mul_f32_e32 v88, 0xbfb8aa3b, v89
	v_exp_f32_e32 v166, v88
	v_cvt_pk_bf16_f32 v88, v175, v177
	v_add_f32_e32 v175, v164, v165
	v_mul_f32_e32 v168, v176, v168
	v_add_f32_e32 v164, 1.0, v166
	v_rcp_f32_e32 v166, v164
	v_pk_mul_f32 v[164:165], v[94:95], v[140:141]
	v_fma_f32 v121, v17, v121, v29
	v_add_f32_e32 v164, v169, v164
	v_mul_f32_e32 v89, v89, v166
	v_mul_f32_e32 v166, 0xbfb8aa3b, v171
	v_exp_f32_e32 v166, v166
	v_add_f32_e32 v169, v164, v165
	v_pk_mul_f32 v[164:165], v[4:5], v[146:147]
	v_cvt_pk_bf16_f32 v89, v168, v89
	global_store_dwordx4 v[160:161], v[86:89], off nt
	v_add_f32_e32 v164, v170, v164
	v_mul_f32_e32 v160, 0xbfb8aa3b, v174
	v_add_f32_e32 v86, v164, v165
	v_add_f32_e32 v87, 1.0, v166
	v_mul_f32_e32 v88, 0xbfb8aa3b, v172
	v_mul_f32_e32 v89, 0xbfb8aa3b, v173
	v_exp_f32_e32 v160, v160
	v_mul_f32_e32 v161, 0xbfb8aa3b, v167
	v_mul_f32_e32 v166, 0xbfb8aa3b, v86
	v_exp_f32_e32 v88, v88
	v_exp_f32_e32 v89, v89
	v_exp_f32_e32 v161, v161
	v_mul_f32_e32 v164, 0xbfb8aa3b, v175
	v_exp_f32_e32 v166, v166
	v_exp_f32_e32 v164, v164
	v_mul_f32_e32 v165, 0xbfb8aa3b, v169
	v_add_f32_e32 v160, 1.0, v160
	v_exp_f32_e32 v165, v165
	v_rcp_f32_e32 v87, v87
	v_add_f32_e32 v88, 1.0, v88
	v_add_f32_e32 v89, 1.0, v89
	v_rcp_f32_e32 v160, v160
	v_add_f32_e32 v161, 1.0, v161
	v_add_f32_e32 v166, 1.0, v166
	v_rcp_f32_e32 v88, v88
	v_rcp_f32_e32 v89, v89
	v_rcp_f32_e32 v161, v161
	v_add_f32_e32 v164, 1.0, v164
	v_rcp_f32_e32 v166, v166
	v_rcp_f32_e32 v164, v164
	v_add_f32_e32 v165, 1.0, v165
	v_mul_f32_e32 v87, v171, v87
	v_mul_f32_e32 v160, v174, v160
	v_rcp_f32_e32 v165, v165
	v_mul_f32_e32 v88, v172, v88
	v_mul_f32_e32 v89, v173, v89
	v_mul_f32_e32 v161, v167, v161
	v_mul_f32_e32 v166, v86, v166
	v_cvt_pk_bf16_f32 v86, v87, v88
	v_cvt_pk_bf16_f32 v87, v89, v160
	v_or_b32_e32 v160, 2, v131
	v_mul_f32_e32 v164, v175, v164
	v_cvt_pk_bf16_f32 v88, v161, v164
	v_mad_i64_i32 v[160:161], s[6:7], v160, s35, v[96:97]
	v_lshl_add_u64 v[160:161], v[160:161], 0, v[110:111]
	v_mul_f32_e32 v165, v169, v165
	v_cvt_pk_bf16_f32 v89, v165, v166
	global_store_dwordx4 v[160:161], v[86:89], off nt
	s_nop 1
	v_fma_f32 v88, v18, v124, v30
	v_pk_mul_f32 v[86:87], v[126:127], v[150:151]
	v_fma_f32 v89, v19, v128, v31
	v_add_f32_e32 v86, v88, v86
	v_fma_f32 v128, v21, v138, v33
	v_fma_f32 v138, v15, v144, v27
	v_add_f32_e32 v144, v86, v87
	v_pk_mul_f32 v[86:87], v[22:23], v[152:153]
	v_fma_f32 v124, v20, v136, v32
	v_add_f32_e32 v86, v89, v86
	v_fma_f32 v136, v14, v142, v26
	v_fma_f32 v142, v16, v148, v28
	v_add_f32_e32 v148, v86, v87
	v_pk_mul_f32 v[86:87], v[106:107], v[154:155]
	v_fma_f32 v88, v18, v125, v30
	v_add_f32_e32 v86, v124, v86
	v_add_f32_e32 v124, v86, v87
	v_pk_mul_f32 v[86:87], v[24:25], v[90:91]
	v_fma_f32 v89, v19, v129, v31
	v_add_f32_e32 v86, v128, v86
	v_add_f32_e32 v128, v86, v87
	v_pk_mul_f32 v[86:87], v[108:109], v[156:157]
	v_fma_f32 v90, v20, v137, v32
	v_add_f32_e32 v86, v136, v86
	v_add_f32_e32 v136, v86, v87
	v_pk_mul_f32 v[86:87], v[10:11], v[158:159]
	v_fma_f32 v91, v21, v139, v33
	v_add_f32_e32 v86, v138, v86
	v_add_f32_e32 v154, v86, v87
	v_pk_mul_f32 v[86:87], v[102:103], v[162:163]
	s_nop 0
	v_add_f32_e32 v86, v142, v86
	v_add_f32_e32 v156, v86, v87
	v_pk_mul_f32 v[86:87], v[12:13], v[92:93]
	v_fma_f32 v92, v14, v143, v26
	v_add_f32_e32 v86, v120, v86
	v_add_f32_e32 v158, v86, v87
	v_or_b32_e32 v86, 3, v131
	v_mad_i64_i32 v[86:87], s[6:7], v86, s35, v[96:97]
	v_lshl_add_u64 v[150:151], v[86:87], 0, v[110:111]
	v_pk_mul_f32 v[86:87], v[126:127], v[112:113]
	v_fma_f32 v93, v15, v145, v27
	v_add_f32_e32 v86, v88, v86
	v_add_f32_e32 v125, v86, v87
	v_pk_mul_f32 v[86:87], v[22:23], v[114:115]
	v_fma_f32 v120, v16, v149, v28
	v_add_f32_e32 v86, v89, v86
	v_add_f32_e32 v129, v86, v87
	v_pk_mul_f32 v[86:87], v[106:107], v[116:117]
	v_pk_mul_f32 v[88:89], v[102:103], v[140:141]
	v_add_f32_e32 v86, v90, v86
	v_add_f32_e32 v137, v86, v87
	v_pk_mul_f32 v[86:87], v[24:25], v[118:119]
	v_add_f32_e32 v88, v120, v88
	v_add_f32_e32 v86, v91, v86
	v_add_f32_e32 v152, v86, v87
	v_pk_mul_f32 v[86:87], v[108:109], v[122:123]
	v_add_f32_e32 v160, v88, v89
	v_add_f32_e32 v86, v92, v86
	v_add_f32_e32 v155, v86, v87
	v_pk_mul_f32 v[86:87], v[10:11], v[134:135]
	v_and_b32_e32 v89, 0xffff0000, v82
	v_add_f32_e32 v86, v93, v86
	v_add_f32_e32 v159, v86, v87
	v_lshlrev_b32_e32 v87, 16, v82
	v_lshlrev_b32_e32 v86, 16, v78
	v_pk_mov_b32 v[138:139], v[112:113], v[86:87] op_sel:[1,0]
	s_nop 0
	v_pk_mul_f32 v[90:91], v[104:105], v[138:139]
	s_nop 0
	v_add_f32_e32 v90, v144, v90
	v_add_f32_e32 v144, v90, v91
	v_mul_f32_e32 v90, 0xbfb8aa3b, v144
	v_exp_f32_e32 v92, v90
	v_pk_mul_f32 v[90:91], v[12:13], v[146:147]
	v_add_f32_e32 v88, 1.0, v92
	v_rcp_f32_e32 v120, v88
	v_and_b32_e32 v88, 0xffff0000, v78
	v_pk_mov_b32 v[142:143], v[114:115], v[88:89] op_sel:[1,0]
	v_add_f32_e32 v90, v121, v90
	v_pk_mul_f32 v[92:93], v[6:7], v[142:143]
	v_add_f32_e32 v161, v90, v91
	v_add_f32_e32 v78, v148, v92
	v_add_f32_e32 v78, v78, v93
	v_mul_f32_e32 v82, 0xbfb8aa3b, v78
	v_exp_f32_e32 v82, v82
	v_pk_mul_f32 v[90:91], v[104:105], v[86:87]
	v_mul_f32_e32 v148, v144, v120
	v_add_f32_e32 v90, v125, v90
	v_add_f32_e32 v82, 1.0, v82
	v_rcp_f32_e32 v82, v82
	v_add_f32_e32 v162, v90, v91
	v_lshlrev_b32_e32 v90, 16, v79
	v_lshlrev_b32_e32 v91, 16, v83
	v_pk_mov_b32 v[144:145], v[116:117], v[90:91] op_sel:[1,0]
	v_mul_f32_e32 v78, v78, v82
	v_pk_mul_f32 v[120:121], v[98:99], v[144:145]
	v_pk_mul_f32 v[92:93], v[6:7], v[88:89]
	v_add_f32_e32 v82, v124, v120
	v_add_f32_e32 v124, v82, v121
	v_mul_f32_e32 v82, 0xbfb8aa3b, v124
	v_exp_f32_e32 v82, v82
	v_add_f32_e32 v92, v129, v92
	v_add_f32_e32 v163, v92, v93
	v_and_b32_e32 v93, 0xffff0000, v83
	v_add_f32_e32 v82, 1.0, v82
	v_and_b32_e32 v92, 0xffff0000, v79
	v_rcp_f32_e32 v125, v82
	v_pk_mov_b32 v[82:83], v[118:119], v[92:93] op_sel:[1,0]
	v_cvt_pk_bf16_f32 v78, v148, v78
	v_mul_f32_e32 v153, v124, v125
	v_pk_mul_f32 v[120:121], v[8:9], v[82:83]
	v_pk_mul_f32 v[124:125], v[98:99], v[90:91]
	v_add_f32_e32 v79, v128, v120
	v_add_f32_e32 v79, v79, v121
	v_mul_f32_e32 v120, 0xbfb8aa3b, v79
	v_exp_f32_e32 v120, v120
	v_add_f32_e32 v124, v137, v124
	v_lshlrev_b32_e32 v121, 16, v84
	v_add_f32_e32 v164, v124, v125
	v_add_f32_e32 v120, 1.0, v120
	v_rcp_f32_e32 v137, v120
	v_lshlrev_b32_e32 v120, 16, v80
	v_pk_mov_b32 v[148:149], v[122:123], v[120:121] op_sel:[1,0]
	v_pk_mul_f32 v[124:125], v[8:9], v[92:93]
	v_pk_mul_f32 v[128:129], v[100:101], v[148:149]
	v_add_f32_e32 v124, v152, v124
	v_add_f32_e32 v128, v136, v128
	v_add_f32_e32 v128, v128, v129
	v_mul_f32_e32 v129, 0xbfb8aa3b, v128
	v_exp_f32_e32 v129, v129
	v_mul_f32_e32 v79, v79, v137
	v_add_f32_e32 v165, v124, v125
	v_and_b32_e32 v125, 0xffff0000, v84
	v_add_f32_e32 v129, 1.0, v129
	v_rcp_f32_e32 v129, v129
	v_and_b32_e32 v124, 0xffff0000, v80
	v_cvt_pk_bf16_f32 v79, v153, v79
	v_pk_mov_b32 v[152:153], v[134:135], v[124:125] op_sel:[1,0]
	v_mul_f32_e32 v166, v128, v129
	v_pk_mul_f32 v[128:129], v[2:3], v[152:153]
	s_nop 0
	v_add_f32_e32 v80, v154, v128
	v_add_f32_e32 v80, v80, v129
	v_pk_mul_f32 v[128:129], v[100:101], v[120:121]
	v_mul_f32_e32 v84, 0xbfb8aa3b, v80
	v_add_f32_e32 v128, v155, v128
	v_add_f32_e32 v167, v128, v129
	v_lshlrev_b32_e32 v128, 16, v81
	v_lshlrev_b32_e32 v129, 16, v85
	v_exp_f32_e32 v84, v84
	v_pk_mov_b32 v[154:155], v[140:141], v[128:129] op_sel:[1,0]
	v_add_f32_e32 v84, 1.0, v84
	v_pk_mul_f32 v[136:137], v[94:95], v[154:155]
	v_rcp_f32_e32 v84, v84
	v_add_f32_e32 v136, v156, v136
	v_add_f32_e32 v168, v136, v137
	v_mul_f32_e32 v136, 0xbfb8aa3b, v168
	v_exp_f32_e32 v136, v136
	v_mul_f32_e32 v169, v80, v84
	v_and_b32_e32 v137, 0xffff0000, v85
	v_pk_mul_f32 v[156:157], v[2:3], v[124:125]
	v_add_f32_e32 v80, 1.0, v136
	v_and_b32_e32 v136, 0xffff0000, v81
	v_pk_mov_b32 v[84:85], v[146:147], v[136:137] op_sel:[1,0]
	v_add_f32_e32 v156, v159, v156
	v_rcp_f32_e32 v159, v80
	v_pk_mul_f32 v[80:81], v[4:5], v[84:85]
	v_mul_f32_e32 v159, v168, v159
	v_add_f32_e32 v80, v158, v80
	v_add_f32_e32 v81, v80, v81
	v_mul_f32_e32 v80, 0xbfb8aa3b, v81
	v_exp_f32_e32 v158, v80
	v_cvt_pk_bf16_f32 v80, v166, v169
	v_add_f32_e32 v166, v156, v157
	v_add_f32_e32 v156, 1.0, v158
	v_rcp_f32_e32 v158, v156
	v_pk_mul_f32 v[156:157], v[94:95], v[128:129]
	v_mul_f32_e32 v81, v81, v158
	v_mul_f32_e32 v158, 0xbfb8aa3b, v162
	v_add_f32_e32 v156, v160, v156
	v_exp_f32_e32 v158, v158
	v_add_f32_e32 v160, v156, v157
	v_pk_mul_f32 v[156:157], v[4:5], v[136:137]
	v_cvt_pk_bf16_f32 v81, v159, v81
	global_store_dwordx4 v[150:151], v[78:81], off nt
	v_add_f32_e32 v156, v161, v156
	v_mul_f32_e32 v150, 0xbfb8aa3b, v165
	v_add_f32_e32 v78, v156, v157
	v_add_f32_e32 v79, 1.0, v158
	v_mul_f32_e32 v80, 0xbfb8aa3b, v163
	v_mul_f32_e32 v81, 0xbfb8aa3b, v164
	v_exp_f32_e32 v150, v150
	v_mul_f32_e32 v151, 0xbfb8aa3b, v167
	v_mul_f32_e32 v158, 0xbfb8aa3b, v78
	v_exp_f32_e32 v80, v80
	v_exp_f32_e32 v81, v81
	v_exp_f32_e32 v151, v151
	v_mul_f32_e32 v156, 0xbfb8aa3b, v166
	v_exp_f32_e32 v158, v158
	v_exp_f32_e32 v156, v156
	v_mul_f32_e32 v157, 0xbfb8aa3b, v160
	v_add_f32_e32 v150, 1.0, v150
	v_exp_f32_e32 v157, v157
	v_rcp_f32_e32 v79, v79
	v_add_f32_e32 v80, 1.0, v80
	v_add_f32_e32 v81, 1.0, v81
	v_rcp_f32_e32 v150, v150
	v_add_f32_e32 v151, 1.0, v151
	v_add_f32_e32 v158, 1.0, v158
	v_rcp_f32_e32 v80, v80
	v_rcp_f32_e32 v81, v81
	v_rcp_f32_e32 v151, v151
	v_add_f32_e32 v156, 1.0, v156
	v_rcp_f32_e32 v158, v158
	v_rcp_f32_e32 v156, v156
	v_add_f32_e32 v157, 1.0, v157
	v_mul_f32_e32 v79, v162, v79
	v_mul_f32_e32 v150, v165, v150
	v_rcp_f32_e32 v157, v157
	v_mul_f32_e32 v80, v163, v80
	v_mul_f32_e32 v81, v164, v81
	v_mul_f32_e32 v151, v167, v151
	v_mul_f32_e32 v158, v78, v158
	v_cvt_pk_bf16_f32 v78, v79, v80
	v_cvt_pk_bf16_f32 v79, v81, v150
	v_or_b32_e32 v150, 4, v131
	v_mul_f32_e32 v156, v166, v156
	v_cvt_pk_bf16_f32 v80, v151, v156
	v_mad_i64_i32 v[150:151], s[6:7], v150, s35, v[96:97]
	v_lshl_add_u64 v[150:151], v[150:151], 0, v[110:111]
	v_mul_f32_e32 v157, v160, v157
	v_cvt_pk_bf16_f32 v81, v157, v158
	global_store_dwordx4 v[150:151], v[78:81], off nt
	s_nop 1
	v_fma_f32 v80, v18, v112, v30
	v_pk_mul_f32 v[78:79], v[126:127], v[138:139]
	v_fma_f32 v81, v19, v114, v31
	v_add_f32_e32 v78, v80, v78
	v_fma_f32 v112, v20, v116, v32
	v_fma_f32 v116, v14, v122, v26
	v_fma_f32 v122, v16, v140, v28
	v_add_f32_e32 v140, v78, v79
	v_pk_mul_f32 v[78:79], v[22:23], v[142:143]
	v_fma_f32 v114, v21, v118, v33
	v_add_f32_e32 v78, v81, v78
	v_add_f32_e32 v142, v78, v79
	v_pk_mul_f32 v[78:79], v[106:107], v[144:145]
	v_fma_f32 v118, v15, v134, v27
	v_add_f32_e32 v78, v112, v78
	v_add_f32_e32 v143, v78, v79
	v_pk_mul_f32 v[78:79], v[24:25], v[82:83]
	v_fma_f32 v134, v17, v146, v29
	v_add_f32_e32 v78, v114, v78
	v_add_f32_e32 v114, v78, v79
	v_pk_mul_f32 v[78:79], v[108:109], v[148:149]
	v_fma_f32 v80, v18, v113, v30
	v_add_f32_e32 v78, v116, v78
	v_add_f32_e32 v144, v78, v79
	v_pk_mul_f32 v[78:79], v[10:11], v[152:153]
	v_fma_f32 v81, v19, v115, v31
	v_add_f32_e32 v78, v118, v78
	v_add_f32_e32 v118, v78, v79
	v_pk_mul_f32 v[78:79], v[102:103], v[154:155]
	v_fma_f32 v82, v20, v117, v32
	v_add_f32_e32 v78, v122, v78
	v_add_f32_e32 v148, v78, v79
	v_pk_mul_f32 v[78:79], v[12:13], v[84:85]
	v_fma_f32 v83, v21, v119, v33
	v_add_f32_e32 v78, v134, v78
	v_add_f32_e32 v150, v78, v79
	v_or_b32_e32 v78, 5, v131
	v_mad_i64_i32 v[78:79], s[6:7], v78, s35, v[96:97]
	v_lshl_add_u64 v[138:139], v[78:79], 0, v[110:111]
	v_pk_mul_f32 v[78:79], v[126:127], v[86:87]
	v_fma_f32 v84, v14, v123, v26
	v_add_f32_e32 v78, v80, v78
	v_add_f32_e32 v115, v78, v79
	v_pk_mul_f32 v[78:79], v[22:23], v[88:89]
	v_fma_f32 v85, v15, v135, v27
	v_add_f32_e32 v78, v81, v78
	v_add_f32_e32 v116, v78, v79
	v_pk_mul_f32 v[78:79], v[106:107], v[90:91]
	v_fma_f32 v112, v16, v141, v28
	v_add_f32_e32 v78, v82, v78
	v_add_f32_e32 v117, v78, v79
	v_pk_mul_f32 v[78:79], v[24:25], v[92:93]
	v_pk_mul_f32 v[80:81], v[102:103], v[128:129]
	v_add_f32_e32 v78, v83, v78
	v_add_f32_e32 v119, v78, v79
	v_pk_mul_f32 v[78:79], v[108:109], v[120:121]
	v_add_f32_e32 v80, v112, v80
	v_add_f32_e32 v78, v84, v78
	v_add_f32_e32 v146, v78, v79
	v_pk_mul_f32 v[78:79], v[10:11], v[124:125]
	v_add_f32_e32 v152, v80, v81
	v_add_f32_e32 v78, v85, v78
	v_add_f32_e32 v151, v78, v79
	v_lshlrev_b32_e32 v79, 16, v74
	v_lshlrev_b32_e32 v78, 16, v70
	v_pk_mov_b32 v[122:123], v[86:87], v[78:79] op_sel:[1,0]
	v_and_b32_e32 v81, 0xffff0000, v74
	v_pk_mul_f32 v[82:83], v[104:105], v[122:123]
	v_fma_f32 v113, v17, v147, v29
	v_add_f32_e32 v82, v140, v82
	v_add_f32_e32 v140, v82, v83
	v_mul_f32_e32 v82, 0xbfb8aa3b, v140
	v_exp_f32_e32 v84, v82
	v_pk_mul_f32 v[82:83], v[12:13], v[136:137]
	v_add_f32_e32 v80, 1.0, v84
	v_rcp_f32_e32 v112, v80
	v_and_b32_e32 v80, 0xffff0000, v70
	v_pk_mov_b32 v[134:135], v[88:89], v[80:81] op_sel:[1,0]
	v_add_f32_e32 v82, v113, v82
	v_pk_mul_f32 v[84:85], v[6:7], v[134:135]
	v_add_f32_e32 v153, v82, v83
	v_add_f32_e32 v70, v142, v84
	v_add_f32_e32 v70, v70, v85
	v_mul_f32_e32 v74, 0xbfb8aa3b, v70
	v_exp_f32_e32 v74, v74
	v_pk_mul_f32 v[82:83], v[104:105], v[78:79]
	v_mul_f32_e32 v142, v140, v112
	v_add_f32_e32 v82, v115, v82
	v_add_f32_e32 v74, 1.0, v74
	v_rcp_f32_e32 v74, v74
	v_add_f32_e32 v154, v82, v83
	v_lshlrev_b32_e32 v82, 16, v71
	v_lshlrev_b32_e32 v83, 16, v75
	v_pk_mov_b32 v[140:141], v[90:91], v[82:83] op_sel:[1,0]
	v_mul_f32_e32 v70, v70, v74
	v_pk_mul_f32 v[112:113], v[98:99], v[140:141]
	v_pk_mul_f32 v[84:85], v[6:7], v[80:81]
	v_add_f32_e32 v74, v143, v112
	v_add_f32_e32 v115, v74, v113
	v_mul_f32_e32 v74, 0xbfb8aa3b, v115
	v_exp_f32_e32 v74, v74
	v_add_f32_e32 v84, v116, v84
	v_add_f32_e32 v155, v84, v85
	v_and_b32_e32 v85, 0xffff0000, v75
	v_add_f32_e32 v74, 1.0, v74
	v_and_b32_e32 v84, 0xffff0000, v71
	v_rcp_f32_e32 v116, v74
	v_pk_mov_b32 v[74:75], v[92:93], v[84:85] op_sel:[1,0]
	v_cvt_pk_bf16_f32 v70, v142, v70
	v_mul_f32_e32 v145, v115, v116
	v_pk_mul_f32 v[112:113], v[8:9], v[74:75]
	s_nop 0
	v_add_f32_e32 v71, v114, v112
	v_add_f32_e32 v71, v71, v113
	v_mul_f32_e32 v112, 0xbfb8aa3b, v71
	v_exp_f32_e32 v112, v112
	v_lshlrev_b32_e32 v113, 16, v76
	v_pk_mul_f32 v[114:115], v[98:99], v[82:83]
	v_add_f32_e32 v112, 1.0, v112
	v_rcp_f32_e32 v147, v112
	v_lshlrev_b32_e32 v112, 16, v72
	v_pk_mov_b32 v[142:143], v[120:121], v[112:113] op_sel:[1,0]
	v_add_f32_e32 v114, v117, v114
	v_pk_mul_f32 v[116:117], v[100:101], v[142:143]
	v_add_f32_e32 v156, v114, v115
	v_add_f32_e32 v116, v144, v116
	v_add_f32_e32 v116, v116, v117
	v_mul_f32_e32 v117, 0xbfb8aa3b, v116
	v_exp_f32_e32 v117, v117
	v_pk_mul_f32 v[114:115], v[8:9], v[84:85]
	v_mul_f32_e32 v71, v71, v147
	v_add_f32_e32 v114, v119, v114
	v_add_f32_e32 v117, 1.0, v117
	v_rcp_f32_e32 v117, v117
	v_add_f32_e32 v157, v114, v115
	v_and_b32_e32 v115, 0xffff0000, v76
	v_and_b32_e32 v114, 0xffff0000, v72
	v_cvt_pk_bf16_f32 v71, v145, v71
	v_pk_mov_b32 v[144:145], v[124:125], v[114:115] op_sel:[1,0]
	v_mul_f32_e32 v158, v116, v117
	v_pk_mul_f32 v[116:117], v[2:3], v[144:145]
	s_nop 0
	v_add_f32_e32 v72, v118, v116
	v_add_f32_e32 v72, v72, v117
	v_pk_mul_f32 v[116:117], v[100:101], v[112:113]
	v_mul_f32_e32 v76, 0xbfb8aa3b, v72
	v_add_f32_e32 v116, v146, v116
	v_add_f32_e32 v159, v116, v117
	v_lshlrev_b32_e32 v116, 16, v73
	v_lshlrev_b32_e32 v117, 16, v77
	v_exp_f32_e32 v76, v76
	v_pk_mov_b32 v[146:147], v[128:129], v[116:117] op_sel:[1,0]
	v_add_f32_e32 v76, 1.0, v76
	v_pk_mul_f32 v[118:119], v[94:95], v[146:147]
	v_rcp_f32_e32 v76, v76
	v_add_f32_e32 v118, v148, v118
	v_add_f32_e32 v160, v118, v119
	v_mul_f32_e32 v118, 0xbfb8aa3b, v160
	v_exp_f32_e32 v118, v118
	v_mul_f32_e32 v161, v72, v76
	v_and_b32_e32 v119, 0xffff0000, v77
	v_pk_mul_f32 v[148:149], v[2:3], v[114:115]
	v_add_f32_e32 v72, 1.0, v118
	v_and_b32_e32 v118, 0xffff0000, v73
	v_pk_mov_b32 v[76:77], v[136:137], v[118:119] op_sel:[1,0]
	v_add_f32_e32 v148, v151, v148
	v_rcp_f32_e32 v151, v72
	v_pk_mul_f32 v[72:73], v[4:5], v[76:77]
	v_mul_f32_e32 v151, v160, v151
	v_add_f32_e32 v72, v150, v72
	v_add_f32_e32 v73, v72, v73
	v_mul_f32_e32 v72, 0xbfb8aa3b, v73
	v_exp_f32_e32 v150, v72
	v_cvt_pk_bf16_f32 v72, v158, v161
	v_add_f32_e32 v158, v148, v149
	v_add_f32_e32 v148, 1.0, v150
	v_rcp_f32_e32 v150, v148
	v_pk_mul_f32 v[148:149], v[94:95], v[116:117]
	v_mul_f32_e32 v73, v73, v150
	v_mul_f32_e32 v150, 0xbfb8aa3b, v154
	v_add_f32_e32 v148, v152, v148
	v_exp_f32_e32 v150, v150
	v_add_f32_e32 v152, v148, v149
	v_pk_mul_f32 v[148:149], v[4:5], v[118:119]
	v_cvt_pk_bf16_f32 v73, v151, v73
	global_store_dwordx4 v[138:139], v[70:73], off nt
	v_add_f32_e32 v148, v153, v148
	v_mul_f32_e32 v138, 0xbfb8aa3b, v157
	v_add_f32_e32 v70, v148, v149
	v_add_f32_e32 v71, 1.0, v150
	v_mul_f32_e32 v72, 0xbfb8aa3b, v155
	v_mul_f32_e32 v73, 0xbfb8aa3b, v156
	v_exp_f32_e32 v138, v138
	v_mul_f32_e32 v139, 0xbfb8aa3b, v159
	v_mul_f32_e32 v150, 0xbfb8aa3b, v70
	v_exp_f32_e32 v72, v72
	v_exp_f32_e32 v73, v73
	v_exp_f32_e32 v139, v139
	v_mul_f32_e32 v148, 0xbfb8aa3b, v158
	v_exp_f32_e32 v150, v150
	v_exp_f32_e32 v148, v148
	v_mul_f32_e32 v149, 0xbfb8aa3b, v152
	v_add_f32_e32 v138, 1.0, v138
	v_exp_f32_e32 v149, v149
	v_rcp_f32_e32 v71, v71
	v_add_f32_e32 v72, 1.0, v72
	v_add_f32_e32 v73, 1.0, v73
	v_rcp_f32_e32 v138, v138
	v_add_f32_e32 v139, 1.0, v139
	v_add_f32_e32 v150, 1.0, v150
	v_rcp_f32_e32 v72, v72
	v_rcp_f32_e32 v73, v73
	v_rcp_f32_e32 v139, v139
	v_add_f32_e32 v148, 1.0, v148
	v_rcp_f32_e32 v150, v150
	v_rcp_f32_e32 v148, v148
	v_add_f32_e32 v149, 1.0, v149
	v_mul_f32_e32 v71, v154, v71
	v_mul_f32_e32 v138, v157, v138
	v_rcp_f32_e32 v149, v149
	v_mul_f32_e32 v72, v155, v72
	v_mul_f32_e32 v73, v156, v73
	v_mul_f32_e32 v139, v159, v139
	v_mul_f32_e32 v150, v70, v150
	v_cvt_pk_bf16_f32 v70, v71, v72
	v_cvt_pk_bf16_f32 v71, v73, v138
	v_or_b32_e32 v138, 6, v131
	v_mul_f32_e32 v148, v158, v148
	v_cvt_pk_bf16_f32 v72, v139, v148
	v_mad_i64_i32 v[138:139], s[6:7], v138, s35, v[96:97]
	v_lshl_add_u64 v[138:139], v[138:139], 0, v[110:111]
	v_mul_f32_e32 v149, v152, v149
	v_cvt_pk_bf16_f32 v73, v149, v150
	global_store_dwordx4 v[138:139], v[70:73], off nt
	s_nop 1
	v_fma_f32 v72, v18, v86, v30
	v_pk_mul_f32 v[70:71], v[126:127], v[122:123]
	v_fma_f32 v73, v19, v88, v31
	v_add_f32_e32 v70, v72, v70
	v_fma_f32 v86, v20, v90, v32
	v_fma_f32 v90, v14, v120, v26
	v_fma_f32 v120, v16, v128, v28
	v_add_f32_e32 v128, v70, v71
	v_pk_mul_f32 v[70:71], v[22:23], v[134:135]
	v_fma_f32 v88, v21, v92, v33
	v_add_f32_e32 v70, v73, v70
	v_add_f32_e32 v134, v70, v71
	v_pk_mul_f32 v[70:71], v[106:107], v[140:141]
	v_fma_f32 v92, v15, v124, v27
	v_add_f32_e32 v70, v86, v70
	v_add_f32_e32 v135, v70, v71
	v_pk_mul_f32 v[70:71], v[24:25], v[74:75]
	v_fma_f32 v124, v17, v136, v29
	v_add_f32_e32 v70, v88, v70
	v_add_f32_e32 v88, v70, v71
	v_pk_mul_f32 v[70:71], v[108:109], v[142:143]
	v_fma_f32 v72, v18, v87, v30
	v_add_f32_e32 v70, v90, v70
	v_add_f32_e32 v136, v70, v71
	v_pk_mul_f32 v[70:71], v[10:11], v[144:145]
	v_fma_f32 v73, v19, v89, v31
	v_add_f32_e32 v70, v92, v70
	v_add_f32_e32 v92, v70, v71
	v_pk_mul_f32 v[70:71], v[102:103], v[146:147]
	v_fma_f32 v74, v20, v91, v32
	v_add_f32_e32 v70, v120, v70
	v_add_f32_e32 v140, v70, v71
	v_pk_mul_f32 v[70:71], v[12:13], v[76:77]
	v_fma_f32 v75, v21, v93, v33
	v_add_f32_e32 v70, v124, v70
	v_add_f32_e32 v142, v70, v71
	v_or_b32_e32 v70, 7, v131
	v_mad_i64_i32 v[70:71], s[6:7], v70, s35, v[96:97]
	v_lshl_add_u64 v[122:123], v[70:71], 0, v[110:111]
	v_pk_mul_f32 v[70:71], v[126:127], v[78:79]
	v_fma_f32 v76, v14, v121, v26
	v_add_f32_e32 v70, v72, v70
	v_add_f32_e32 v89, v70, v71
	v_pk_mul_f32 v[70:71], v[22:23], v[80:81]
	v_fma_f32 v77, v15, v125, v27
	v_add_f32_e32 v70, v73, v70
	v_add_f32_e32 v90, v70, v71
	v_pk_mul_f32 v[70:71], v[106:107], v[82:83]
	v_fma_f32 v86, v16, v129, v28
	v_add_f32_e32 v70, v74, v70
	v_add_f32_e32 v91, v70, v71
	v_pk_mul_f32 v[70:71], v[24:25], v[84:85]
	v_pk_mul_f32 v[72:73], v[102:103], v[116:117]
	v_add_f32_e32 v70, v75, v70
	v_add_f32_e32 v93, v70, v71
	v_pk_mul_f32 v[70:71], v[108:109], v[112:113]
	v_add_f32_e32 v72, v86, v72
	v_add_f32_e32 v70, v76, v70
	v_add_f32_e32 v138, v70, v71
	v_pk_mul_f32 v[70:71], v[10:11], v[114:115]
	v_add_f32_e32 v144, v72, v73
	v_add_f32_e32 v70, v77, v70
	v_add_f32_e32 v143, v70, v71
	v_lshlrev_b32_e32 v71, 16, v66
	v_lshlrev_b32_e32 v70, 16, v62
	v_pk_mov_b32 v[120:121], v[78:79], v[70:71] op_sel:[1,0]
	v_and_b32_e32 v73, 0xffff0000, v66
	v_pk_mul_f32 v[74:75], v[104:105], v[120:121]
	v_fma_f32 v87, v17, v137, v29
	v_add_f32_e32 v74, v128, v74
	v_add_f32_e32 v128, v74, v75
	v_mul_f32_e32 v74, 0xbfb8aa3b, v128
	v_exp_f32_e32 v76, v74
	v_pk_mul_f32 v[74:75], v[12:13], v[118:119]
	v_add_f32_e32 v72, 1.0, v76
	v_rcp_f32_e32 v86, v72
	v_and_b32_e32 v72, 0xffff0000, v62
	v_pk_mov_b32 v[124:125], v[80:81], v[72:73] op_sel:[1,0]
	v_add_f32_e32 v74, v87, v74
	v_pk_mul_f32 v[76:77], v[6:7], v[124:125]
	v_add_f32_e32 v145, v74, v75
	v_add_f32_e32 v62, v134, v76
	v_add_f32_e32 v62, v62, v77
	v_mul_f32_e32 v66, 0xbfb8aa3b, v62
	v_exp_f32_e32 v66, v66
	v_pk_mul_f32 v[74:75], v[104:105], v[70:71]
	v_mul_f32_e32 v134, v128, v86
	v_add_f32_e32 v74, v89, v74
	v_add_f32_e32 v66, 1.0, v66
	v_rcp_f32_e32 v66, v66
	v_add_f32_e32 v146, v74, v75
	v_lshlrev_b32_e32 v74, 16, v63
	v_lshlrev_b32_e32 v75, 16, v67
	v_pk_mov_b32 v[128:129], v[82:83], v[74:75] op_sel:[1,0]
	v_mul_f32_e32 v62, v62, v66
	v_pk_mul_f32 v[86:87], v[98:99], v[128:129]
	v_pk_mul_f32 v[76:77], v[6:7], v[72:73]
	v_add_f32_e32 v66, v135, v86
	v_add_f32_e32 v89, v66, v87
	v_mul_f32_e32 v66, 0xbfb8aa3b, v89
	v_exp_f32_e32 v66, v66
	v_add_f32_e32 v76, v90, v76
	v_add_f32_e32 v147, v76, v77
	v_and_b32_e32 v77, 0xffff0000, v67
	v_add_f32_e32 v66, 1.0, v66
	v_and_b32_e32 v76, 0xffff0000, v63
	v_rcp_f32_e32 v90, v66
	v_pk_mov_b32 v[66:67], v[84:85], v[76:77] op_sel:[1,0]
	v_cvt_pk_bf16_f32 v62, v134, v62
	v_mul_f32_e32 v137, v89, v90
	v_pk_mul_f32 v[86:87], v[8:9], v[66:67]
	s_nop 0
	v_add_f32_e32 v63, v88, v86
	v_add_f32_e32 v63, v63, v87
	v_mul_f32_e32 v86, 0xbfb8aa3b, v63
	v_exp_f32_e32 v86, v86
	v_lshlrev_b32_e32 v87, 16, v68
	v_pk_mul_f32 v[88:89], v[98:99], v[74:75]
	v_add_f32_e32 v86, 1.0, v86
	v_rcp_f32_e32 v139, v86
	v_lshlrev_b32_e32 v86, 16, v64
	v_pk_mov_b32 v[134:135], v[112:113], v[86:87] op_sel:[1,0]
	v_add_f32_e32 v88, v91, v88
	v_pk_mul_f32 v[90:91], v[100:101], v[134:135]
	v_add_f32_e32 v148, v88, v89
	v_add_f32_e32 v90, v136, v90
	v_add_f32_e32 v90, v90, v91
	v_mul_f32_e32 v91, 0xbfb8aa3b, v90
	v_exp_f32_e32 v91, v91
	v_pk_mul_f32 v[88:89], v[8:9], v[76:77]
	v_mul_f32_e32 v63, v63, v139
	v_add_f32_e32 v88, v93, v88
	v_add_f32_e32 v91, 1.0, v91
	v_rcp_f32_e32 v91, v91
	v_add_f32_e32 v149, v88, v89
	v_and_b32_e32 v89, 0xffff0000, v68
	v_and_b32_e32 v88, 0xffff0000, v64
	v_cvt_pk_bf16_f32 v63, v137, v63
	v_pk_mov_b32 v[136:137], v[114:115], v[88:89] op_sel:[1,0]
	v_mul_f32_e32 v150, v90, v91
	v_pk_mul_f32 v[90:91], v[2:3], v[136:137]
	s_nop 0
	v_add_f32_e32 v64, v92, v90
	v_add_f32_e32 v64, v64, v91
	v_pk_mul_f32 v[90:91], v[100:101], v[86:87]
	v_mul_f32_e32 v68, 0xbfb8aa3b, v64
	v_add_f32_e32 v90, v138, v90
	v_add_f32_e32 v151, v90, v91
	v_lshlrev_b32_e32 v90, 16, v65
	v_lshlrev_b32_e32 v91, 16, v69
	v_exp_f32_e32 v68, v68
	v_pk_mov_b32 v[138:139], v[116:117], v[90:91] op_sel:[1,0]
	v_add_f32_e32 v68, 1.0, v68
	v_pk_mul_f32 v[92:93], v[94:95], v[138:139]
	v_rcp_f32_e32 v68, v68
	v_add_f32_e32 v92, v140, v92
	v_add_f32_e32 v152, v92, v93
	v_mul_f32_e32 v92, 0xbfb8aa3b, v152
	v_exp_f32_e32 v92, v92
	v_mul_f32_e32 v153, v64, v68
	v_and_b32_e32 v93, 0xffff0000, v69
	v_pk_mul_f32 v[140:141], v[2:3], v[88:89]
	v_add_f32_e32 v64, 1.0, v92
	v_and_b32_e32 v92, 0xffff0000, v65
	v_pk_mov_b32 v[68:69], v[118:119], v[92:93] op_sel:[1,0]
	v_add_f32_e32 v140, v143, v140
	v_rcp_f32_e32 v143, v64
	v_pk_mul_f32 v[64:65], v[4:5], v[68:69]
	v_mul_f32_e32 v143, v152, v143
	v_add_f32_e32 v64, v142, v64
	v_add_f32_e32 v65, v64, v65
	v_mul_f32_e32 v64, 0xbfb8aa3b, v65
	v_exp_f32_e32 v142, v64
	v_cvt_pk_bf16_f32 v64, v150, v153
	v_add_f32_e32 v150, v140, v141
	v_add_f32_e32 v140, 1.0, v142
	v_rcp_f32_e32 v142, v140
	v_pk_mul_f32 v[140:141], v[94:95], v[90:91]
	v_mul_f32_e32 v65, v65, v142
	v_mul_f32_e32 v142, 0xbfb8aa3b, v146
	v_add_f32_e32 v140, v144, v140
	v_exp_f32_e32 v142, v142
	v_add_f32_e32 v144, v140, v141
	v_pk_mul_f32 v[140:141], v[4:5], v[92:93]
	v_cvt_pk_bf16_f32 v65, v143, v65
	global_store_dwordx4 v[122:123], v[62:65], off nt
	v_add_f32_e32 v140, v145, v140
	v_mul_f32_e32 v122, 0xbfb8aa3b, v149
	v_add_f32_e32 v62, v140, v141
	v_add_f32_e32 v63, 1.0, v142
	v_mul_f32_e32 v64, 0xbfb8aa3b, v147
	v_mul_f32_e32 v65, 0xbfb8aa3b, v148
	v_exp_f32_e32 v122, v122
	v_mul_f32_e32 v123, 0xbfb8aa3b, v151
	v_mul_f32_e32 v142, 0xbfb8aa3b, v62
	v_exp_f32_e32 v64, v64
	v_exp_f32_e32 v65, v65
	v_exp_f32_e32 v123, v123
	v_mul_f32_e32 v140, 0xbfb8aa3b, v150
	v_exp_f32_e32 v142, v142
	v_exp_f32_e32 v140, v140
	v_mul_f32_e32 v141, 0xbfb8aa3b, v144
	v_add_f32_e32 v122, 1.0, v122
	v_exp_f32_e32 v141, v141
	v_rcp_f32_e32 v63, v63
	v_add_f32_e32 v64, 1.0, v64
	v_add_f32_e32 v65, 1.0, v65
	v_rcp_f32_e32 v122, v122
	v_add_f32_e32 v123, 1.0, v123
	v_add_f32_e32 v142, 1.0, v142
	v_rcp_f32_e32 v64, v64
	v_rcp_f32_e32 v65, v65
	v_rcp_f32_e32 v123, v123
	v_add_f32_e32 v140, 1.0, v140
	v_rcp_f32_e32 v142, v142
	v_rcp_f32_e32 v140, v140
	v_add_f32_e32 v141, 1.0, v141
	v_mul_f32_e32 v63, v146, v63
	v_mul_f32_e32 v122, v149, v122
	v_rcp_f32_e32 v141, v141
	v_mul_f32_e32 v64, v147, v64
	v_mul_f32_e32 v65, v148, v65
	v_mul_f32_e32 v123, v151, v123
	v_mul_f32_e32 v142, v62, v142
	v_cvt_pk_bf16_f32 v62, v63, v64
	v_cvt_pk_bf16_f32 v63, v65, v122
	v_or_b32_e32 v122, 8, v131
	v_mul_f32_e32 v140, v150, v140
	v_cvt_pk_bf16_f32 v64, v123, v140
	v_mad_i64_i32 v[122:123], s[6:7], v122, s35, v[96:97]
	v_lshl_add_u64 v[122:123], v[122:123], 0, v[110:111]
	v_mul_f32_e32 v141, v144, v141
	v_cvt_pk_bf16_f32 v65, v141, v142
	global_store_dwordx4 v[122:123], v[62:65], off nt
	s_nop 1
	v_fma_f32 v64, v18, v78, v30
	v_pk_mul_f32 v[62:63], v[126:127], v[120:121]
	v_fma_f32 v65, v19, v80, v31
	v_add_f32_e32 v62, v64, v62
	v_fma_f32 v78, v20, v82, v32
	v_fma_f32 v82, v14, v112, v26
	v_fma_f32 v112, v16, v116, v28
	v_add_f32_e32 v116, v62, v63
	v_pk_mul_f32 v[62:63], v[22:23], v[124:125]
	v_fma_f32 v80, v21, v84, v33
	v_add_f32_e32 v62, v65, v62
	v_fma_f32 v84, v15, v114, v27
	v_fma_f32 v114, v17, v118, v29
	v_add_f32_e32 v118, v62, v63
	v_pk_mul_f32 v[62:63], v[106:107], v[128:129]
	v_fma_f32 v64, v18, v79, v30
	v_add_f32_e32 v62, v78, v62
	v_add_f32_e32 v122, v62, v63
	v_pk_mul_f32 v[62:63], v[24:25], v[66:67]
	v_fma_f32 v65, v19, v81, v31
	v_add_f32_e32 v62, v80, v62
	v_add_f32_e32 v80, v62, v63
	v_pk_mul_f32 v[62:63], v[108:109], v[134:135]
	v_fma_f32 v66, v20, v83, v32
	v_add_f32_e32 v62, v82, v62
	v_add_f32_e32 v82, v62, v63
	v_pk_mul_f32 v[62:63], v[10:11], v[136:137]
	v_fma_f32 v67, v21, v85, v33
	v_add_f32_e32 v62, v84, v62
	v_add_f32_e32 v124, v62, v63
	v_pk_mul_f32 v[62:63], v[102:103], v[138:139]
	v_fma_f32 v79, v17, v119, v29
	v_add_f32_e32 v62, v112, v62
	v_add_f32_e32 v128, v62, v63
	v_pk_mul_f32 v[62:63], v[12:13], v[68:69]
	v_fma_f32 v68, v14, v113, v26
	v_add_f32_e32 v62, v114, v62
	v_add_f32_e32 v134, v62, v63
	v_or_b32_e32 v62, 9, v131
	v_mad_i64_i32 v[62:63], s[6:7], v62, s35, v[96:97]
	v_lshl_add_u64 v[120:121], v[62:63], 0, v[110:111]
	v_pk_mul_f32 v[62:63], v[126:127], v[70:71]
	v_fma_f32 v69, v15, v115, v27
	v_add_f32_e32 v62, v64, v62
	v_add_f32_e32 v81, v62, v63
	v_pk_mul_f32 v[62:63], v[22:23], v[72:73]
	v_fma_f32 v78, v16, v117, v28
	v_add_f32_e32 v62, v65, v62
	v_add_f32_e32 v83, v62, v63
	v_pk_mul_f32 v[62:63], v[106:107], v[74:75]
	v_pk_mul_f32 v[64:65], v[102:103], v[90:91]
	v_add_f32_e32 v62, v66, v62
	v_add_f32_e32 v119, v62, v63
	v_pk_mul_f32 v[62:63], v[24:25], v[76:77]
	v_add_f32_e32 v64, v78, v64
	v_add_f32_e32 v62, v67, v62
	v_add_f32_e32 v123, v62, v63
	v_pk_mul_f32 v[62:63], v[108:109], v[86:87]
	v_add_f32_e32 v136, v64, v65
	v_add_f32_e32 v62, v68, v62
	v_add_f32_e32 v125, v62, v63
	v_pk_mul_f32 v[62:63], v[10:11], v[88:89]
	v_and_b32_e32 v65, 0xffff0000, v58
	v_add_f32_e32 v62, v69, v62
	v_add_f32_e32 v135, v62, v63
	v_lshlrev_b32_e32 v63, 16, v58
	v_lshlrev_b32_e32 v62, 16, v54
	v_pk_mov_b32 v[84:85], v[70:71], v[62:63] op_sel:[1,0]
	s_nop 0
	v_pk_mul_f32 v[66:67], v[104:105], v[84:85]
	s_nop 0
	v_add_f32_e32 v66, v116, v66
	v_add_f32_e32 v114, v66, v67
	v_mul_f32_e32 v66, 0xbfb8aa3b, v114
	v_exp_f32_e32 v68, v66
	v_pk_mul_f32 v[66:67], v[12:13], v[92:93]
	v_add_f32_e32 v64, 1.0, v68
	v_rcp_f32_e32 v78, v64
	v_and_b32_e32 v64, 0xffff0000, v54
	v_pk_mov_b32 v[112:113], v[72:73], v[64:65] op_sel:[1,0]
	v_add_f32_e32 v66, v79, v66
	v_pk_mul_f32 v[68:69], v[6:7], v[112:113]
	v_add_f32_e32 v137, v66, v67
	v_add_f32_e32 v54, v118, v68
	v_add_f32_e32 v54, v54, v69
	v_mul_f32_e32 v58, 0xbfb8aa3b, v54
	v_exp_f32_e32 v58, v58
	v_pk_mul_f32 v[66:67], v[104:105], v[62:63]
	v_mul_f32_e32 v116, v114, v78
	v_add_f32_e32 v66, v81, v66
	v_add_f32_e32 v58, 1.0, v58
	v_rcp_f32_e32 v58, v58
	v_add_f32_e32 v138, v66, v67
	v_lshlrev_b32_e32 v66, 16, v55
	v_lshlrev_b32_e32 v67, 16, v59
	v_pk_mov_b32 v[114:115], v[74:75], v[66:67] op_sel:[1,0]
	v_mul_f32_e32 v54, v54, v58
	v_pk_mul_f32 v[78:79], v[98:99], v[114:115]
	v_pk_mul_f32 v[68:69], v[6:7], v[64:65]
	v_add_f32_e32 v58, v122, v78
	v_add_f32_e32 v78, v58, v79
	v_mul_f32_e32 v58, 0xbfb8aa3b, v78
	v_exp_f32_e32 v58, v58
	v_and_b32_e32 v59, 0xffff0000, v59
	v_add_f32_e32 v68, v83, v68
	v_cvt_pk_bf16_f32 v54, v116, v54
	v_add_f32_e32 v58, 1.0, v58
	v_rcp_f32_e32 v79, v58
	v_and_b32_e32 v58, 0xffff0000, v55
	v_pk_mov_b32 v[116:117], v[76:77], v[58:59] op_sel:[1,0]
	v_add_f32_e32 v139, v68, v69
	v_pk_mul_f32 v[68:69], v[8:9], v[116:117]
	v_mul_f32_e32 v83, v78, v79
	v_add_f32_e32 v55, v80, v68
	v_add_f32_e32 v55, v55, v69
	v_mul_f32_e32 v68, 0xbfb8aa3b, v55
	v_exp_f32_e32 v68, v68
	v_pk_mul_f32 v[78:79], v[98:99], v[66:67]
	v_lshlrev_b32_e32 v69, 16, v60
	v_add_f32_e32 v78, v119, v78
	v_add_f32_e32 v68, 1.0, v68
	v_rcp_f32_e32 v122, v68
	v_lshlrev_b32_e32 v68, 16, v56
	v_pk_mov_b32 v[118:119], v[86:87], v[68:69] op_sel:[1,0]
	v_add_f32_e32 v140, v78, v79
	v_pk_mul_f32 v[80:81], v[100:101], v[118:119]
	v_pk_mul_f32 v[78:79], v[8:9], v[58:59]
	v_add_f32_e32 v80, v82, v80
	v_add_f32_e32 v80, v80, v81
	v_mul_f32_e32 v81, 0xbfb8aa3b, v80
	v_exp_f32_e32 v81, v81
	v_add_f32_e32 v78, v123, v78
	v_add_f32_e32 v141, v78, v79
	v_and_b32_e32 v79, 0xffff0000, v60
	v_add_f32_e32 v81, 1.0, v81
	v_rcp_f32_e32 v81, v81
	v_and_b32_e32 v78, 0xffff0000, v56
	v_mul_f32_e32 v55, v55, v122
	v_pk_mov_b32 v[122:123], v[88:89], v[78:79] op_sel:[1,0]
	v_mul_f32_e32 v142, v80, v81
	v_pk_mul_f32 v[80:81], v[2:3], v[122:123]
	v_cvt_pk_bf16_f32 v55, v83, v55
	s_nop 0
	v_add_f32_e32 v56, v124, v80
	v_add_f32_e32 v56, v56, v81
	v_pk_mul_f32 v[80:81], v[100:101], v[68:69]
	v_mul_f32_e32 v60, 0xbfb8aa3b, v56
	v_add_f32_e32 v80, v125, v80
	v_add_f32_e32 v143, v80, v81
	v_lshlrev_b32_e32 v80, 16, v57
	v_lshlrev_b32_e32 v81, 16, v61
	v_exp_f32_e32 v60, v60
	v_pk_mov_b32 v[124:125], v[90:91], v[80:81] op_sel:[1,0]
	v_add_f32_e32 v60, 1.0, v60
	v_pk_mul_f32 v[82:83], v[94:95], v[124:125]
	v_rcp_f32_e32 v60, v60
	v_add_f32_e32 v82, v128, v82
	v_add_f32_e32 v144, v82, v83
	v_mul_f32_e32 v82, 0xbfb8aa3b, v144
	v_exp_f32_e32 v82, v82
	v_mul_f32_e32 v145, v56, v60
	v_and_b32_e32 v83, 0xffff0000, v61
	v_pk_mul_f32 v[128:129], v[2:3], v[78:79]
	v_add_f32_e32 v56, 1.0, v82
	v_and_b32_e32 v82, 0xffff0000, v57
	v_pk_mov_b32 v[60:61], v[92:93], v[82:83] op_sel:[1,0]
	v_add_f32_e32 v128, v135, v128
	v_rcp_f32_e32 v135, v56
	v_pk_mul_f32 v[56:57], v[4:5], v[60:61]
	v_mul_f32_e32 v135, v144, v135
	v_add_f32_e32 v56, v134, v56
	v_add_f32_e32 v57, v56, v57
	v_mul_f32_e32 v56, 0xbfb8aa3b, v57
	v_exp_f32_e32 v134, v56
	v_cvt_pk_bf16_f32 v56, v142, v145
	v_add_f32_e32 v142, v128, v129
	v_add_f32_e32 v128, 1.0, v134
	v_rcp_f32_e32 v134, v128
	v_pk_mul_f32 v[128:129], v[94:95], v[80:81]
	v_mul_f32_e32 v57, v57, v134
	v_mul_f32_e32 v134, 0xbfb8aa3b, v138
	v_add_f32_e32 v128, v136, v128
	v_exp_f32_e32 v134, v134
	v_add_f32_e32 v136, v128, v129
	v_pk_mul_f32 v[128:129], v[4:5], v[82:83]
	v_cvt_pk_bf16_f32 v57, v135, v57
	global_store_dwordx4 v[120:121], v[54:57], off nt
	v_add_f32_e32 v128, v137, v128
	v_mul_f32_e32 v120, 0xbfb8aa3b, v141
	v_add_f32_e32 v54, v128, v129
	v_add_f32_e32 v55, 1.0, v134
	v_mul_f32_e32 v56, 0xbfb8aa3b, v139
	v_mul_f32_e32 v57, 0xbfb8aa3b, v140
	v_exp_f32_e32 v120, v120
	v_mul_f32_e32 v121, 0xbfb8aa3b, v143
	v_mul_f32_e32 v134, 0xbfb8aa3b, v54
	v_exp_f32_e32 v56, v56
	v_exp_f32_e32 v57, v57
	v_exp_f32_e32 v121, v121
	v_mul_f32_e32 v128, 0xbfb8aa3b, v142
	v_exp_f32_e32 v134, v134
	v_exp_f32_e32 v128, v128
	v_mul_f32_e32 v129, 0xbfb8aa3b, v136
	v_add_f32_e32 v120, 1.0, v120
	v_exp_f32_e32 v129, v129
	v_rcp_f32_e32 v55, v55
	v_add_f32_e32 v56, 1.0, v56
	v_add_f32_e32 v57, 1.0, v57
	v_rcp_f32_e32 v120, v120
	v_add_f32_e32 v121, 1.0, v121
	v_add_f32_e32 v134, 1.0, v134
	v_rcp_f32_e32 v56, v56
	v_rcp_f32_e32 v57, v57
	v_rcp_f32_e32 v121, v121
	v_add_f32_e32 v128, 1.0, v128
	v_rcp_f32_e32 v134, v134
	v_rcp_f32_e32 v128, v128
	v_add_f32_e32 v129, 1.0, v129
	v_mul_f32_e32 v55, v138, v55
	v_mul_f32_e32 v120, v141, v120
	v_rcp_f32_e32 v129, v129
	v_mul_f32_e32 v56, v139, v56
	v_mul_f32_e32 v57, v140, v57
	v_mul_f32_e32 v121, v143, v121
	v_mul_f32_e32 v134, v54, v134
	v_cvt_pk_bf16_f32 v54, v55, v56
	v_cvt_pk_bf16_f32 v55, v57, v120
	v_or_b32_e32 v120, 10, v131
	v_mul_f32_e32 v128, v142, v128
	v_cvt_pk_bf16_f32 v56, v121, v128
	v_mad_i64_i32 v[120:121], s[6:7], v120, s35, v[96:97]
	v_lshl_add_u64 v[120:121], v[120:121], 0, v[110:111]
	v_mul_f32_e32 v129, v136, v129
	v_cvt_pk_bf16_f32 v57, v129, v134
	global_store_dwordx4 v[120:121], v[54:57], off nt
	s_nop 1
	v_fma_f32 v56, v18, v70, v30
	v_pk_mul_f32 v[54:55], v[126:127], v[84:85]
	v_fma_f32 v57, v19, v72, v31
	v_add_f32_e32 v54, v56, v54
	v_fma_f32 v70, v20, v74, v32
	v_fma_f32 v74, v14, v86, v26
	v_fma_f32 v86, v16, v90, v28
	v_add_f32_e32 v90, v54, v55
	v_pk_mul_f32 v[54:55], v[22:23], v[112:113]
	v_fma_f32 v72, v21, v76, v33
	v_add_f32_e32 v54, v57, v54
	v_fma_f32 v76, v15, v88, v27
	v_fma_f32 v88, v17, v92, v29
	v_add_f32_e32 v92, v54, v55
	v_pk_mul_f32 v[54:55], v[106:107], v[114:115]
	v_fma_f32 v56, v18, v71, v30
	v_add_f32_e32 v54, v70, v54
	v_add_f32_e32 v112, v54, v55
	v_pk_mul_f32 v[54:55], v[24:25], v[116:117]
	v_fma_f32 v57, v19, v73, v31
	v_add_f32_e32 v54, v72, v54
	v_add_f32_e32 v113, v54, v55
	v_pk_mul_f32 v[54:55], v[108:109], v[118:119]
	v_fma_f32 v70, v14, v87, v26
	v_add_f32_e32 v54, v74, v54
	v_add_f32_e32 v114, v54, v55
	v_pk_mul_f32 v[54:55], v[10:11], v[122:123]
	v_fma_f32 v71, v15, v89, v27
	v_add_f32_e32 v54, v76, v54
	v_add_f32_e32 v76, v54, v55
	v_pk_mul_f32 v[54:55], v[102:103], v[124:125]
	v_fma_f32 v72, v16, v91, v28
	v_add_f32_e32 v54, v86, v54
	v_add_f32_e32 v118, v54, v55
	v_pk_mul_f32 v[54:55], v[12:13], v[60:61]
	v_fma_f32 v60, v20, v75, v32
	v_add_f32_e32 v54, v88, v54
	v_add_f32_e32 v120, v54, v55
	v_or_b32_e32 v54, 11, v131
	v_mad_i64_i32 v[54:55], s[6:7], v54, s35, v[96:97]
	v_lshl_add_u64 v[84:85], v[54:55], 0, v[110:111]
	v_pk_mul_f32 v[54:55], v[126:127], v[62:63]
	v_fma_f32 v61, v21, v77, v33
	v_add_f32_e32 v54, v56, v54
	v_add_f32_e32 v74, v54, v55
	v_pk_mul_f32 v[54:55], v[22:23], v[64:65]
	v_fma_f32 v73, v17, v93, v29
	v_add_f32_e32 v54, v57, v54
	v_add_f32_e32 v75, v54, v55
	v_pk_mul_f32 v[54:55], v[106:107], v[66:67]
	v_pk_mul_f32 v[56:57], v[102:103], v[80:81]
	v_add_f32_e32 v54, v60, v54
	v_add_f32_e32 v77, v54, v55
	v_pk_mul_f32 v[54:55], v[24:25], v[58:59]
	v_add_f32_e32 v56, v72, v56
	v_add_f32_e32 v54, v61, v54
	v_add_f32_e32 v115, v54, v55
	v_pk_mul_f32 v[54:55], v[108:109], v[68:69]
	v_add_f32_e32 v121, v56, v57
	v_add_f32_e32 v54, v70, v54
	v_add_f32_e32 v116, v54, v55
	v_pk_mul_f32 v[54:55], v[10:11], v[78:79]
	v_and_b32_e32 v57, 0xffff0000, v50
	v_add_f32_e32 v54, v71, v54
	v_add_f32_e32 v119, v54, v55
	v_lshlrev_b32_e32 v55, 16, v50
	v_lshlrev_b32_e32 v54, 16, v46
	v_pk_mov_b32 v[86:87], v[62:63], v[54:55] op_sel:[1,0]
	v_fma_f32 v62, v18, v62, v30
	v_pk_mul_f32 v[60:61], v[104:105], v[86:87]
	s_nop 0
	v_add_f32_e32 v60, v90, v60
	v_add_f32_e32 v90, v60, v61
	v_mul_f32_e32 v60, 0xbfb8aa3b, v90
	v_exp_f32_e32 v70, v60
	v_pk_mul_f32 v[60:61], v[12:13], v[82:83]
	v_add_f32_e32 v56, 1.0, v70
	v_rcp_f32_e32 v72, v56
	v_and_b32_e32 v56, 0xffff0000, v46
	v_pk_mov_b32 v[88:89], v[64:65], v[56:57] op_sel:[1,0]
	v_add_f32_e32 v60, v73, v60
	v_pk_mul_f32 v[70:71], v[6:7], v[88:89]
	v_add_f32_e32 v122, v60, v61
	v_add_f32_e32 v46, v92, v70
	v_add_f32_e32 v46, v46, v71
	v_mul_f32_e32 v50, 0xbfb8aa3b, v46
	v_exp_f32_e32 v50, v50
	v_pk_mul_f32 v[60:61], v[104:105], v[54:55]
	v_mul_f32_e32 v92, v90, v72
	v_add_f32_e32 v60, v74, v60
	v_add_f32_e32 v50, 1.0, v50
	v_rcp_f32_e32 v50, v50
	v_add_f32_e32 v123, v60, v61
	v_lshlrev_b32_e32 v60, 16, v47
	v_lshlrev_b32_e32 v61, 16, v51
	v_pk_mov_b32 v[90:91], v[66:67], v[60:61] op_sel:[1,0]
	v_mul_f32_e32 v46, v46, v50
	v_pk_mul_f32 v[72:73], v[98:99], v[90:91]
	v_pk_mul_f32 v[70:71], v[6:7], v[56:57]
	v_add_f32_e32 v50, v112, v72
	v_add_f32_e32 v72, v50, v73
	v_mul_f32_e32 v50, 0xbfb8aa3b, v72
	v_exp_f32_e32 v50, v50
	v_cvt_pk_bf16_f32 v74, v92, v46
	v_and_b32_e32 v51, 0xffff0000, v51
	v_add_f32_e32 v70, v75, v70
	v_add_f32_e32 v46, 1.0, v50
	v_and_b32_e32 v50, 0xffff0000, v47
	v_pk_mov_b32 v[92:93], v[58:59], v[50:51] op_sel:[1,0]
	v_add_f32_e32 v124, v70, v71
	v_rcp_f32_e32 v70, v46
	v_pk_mul_f32 v[46:47], v[8:9], v[92:93]
	v_fma_f32 v64, v19, v64, v31
	v_add_f32_e32 v46, v113, v46
	v_add_f32_e32 v75, v46, v47
	v_mul_f32_e32 v46, 0xbfb8aa3b, v75
	v_exp_f32_e32 v46, v46
	v_mul_f32_e32 v117, v72, v70
	v_pk_mul_f32 v[70:71], v[98:99], v[60:61]
	v_lshlrev_b32_e32 v47, 16, v52
	v_add_f32_e32 v46, 1.0, v46
	v_add_f32_e32 v70, v77, v70
	v_rcp_f32_e32 v77, v46
	v_lshlrev_b32_e32 v46, 16, v48
	v_pk_mov_b32 v[112:113], v[68:69], v[46:47] op_sel:[1,0]
	v_add_f32_e32 v125, v70, v71
	v_pk_mul_f32 v[72:73], v[100:101], v[112:113]
	v_pk_mul_f32 v[70:71], v[8:9], v[50:51]
	v_add_f32_e32 v72, v114, v72
	v_add_f32_e32 v72, v72, v73
	v_mul_f32_e32 v73, 0xbfb8aa3b, v72
	v_exp_f32_e32 v73, v73
	v_add_f32_e32 v70, v115, v70
	v_add_f32_e32 v128, v70, v71
	v_and_b32_e32 v71, 0xffff0000, v52
	v_add_f32_e32 v73, 1.0, v73
	v_rcp_f32_e32 v73, v73
	v_and_b32_e32 v70, 0xffff0000, v48
	v_pk_mov_b32 v[114:115], v[78:79], v[70:71] op_sel:[1,0]
	v_mul_f32_e32 v75, v75, v77
	v_mul_f32_e32 v129, v72, v73
	v_pk_mul_f32 v[72:73], v[2:3], v[114:115]
	v_cvt_pk_bf16_f32 v75, v117, v75
	v_fma_f32 v66, v20, v66, v32
	v_add_f32_e32 v48, v76, v72
	v_add_f32_e32 v48, v48, v73
	v_pk_mul_f32 v[72:73], v[100:101], v[46:47]
	v_mul_f32_e32 v52, 0xbfb8aa3b, v48
	v_add_f32_e32 v72, v116, v72
	v_add_f32_e32 v134, v72, v73
	v_lshlrev_b32_e32 v72, 16, v49
	v_lshlrev_b32_e32 v73, 16, v53
	v_exp_f32_e32 v52, v52
	v_pk_mov_b32 v[116:117], v[80:81], v[72:73] op_sel:[1,0]
	v_and_b32_e32 v53, 0xffff0000, v53
	v_pk_mul_f32 v[76:77], v[94:95], v[116:117]
	v_add_f32_e32 v52, 1.0, v52
	v_add_f32_e32 v76, v118, v76
	v_add_f32_e32 v135, v76, v77
	v_mul_f32_e32 v76, 0xbfb8aa3b, v135
	v_rcp_f32_e32 v52, v52
	v_exp_f32_e32 v118, v76
	v_pk_mul_f32 v[76:77], v[2:3], v[70:71]
	v_fma_f32 v58, v21, v58, v33
	v_mul_f32_e32 v136, v48, v52
	v_add_f32_e32 v48, 1.0, v118
	v_and_b32_e32 v52, 0xffff0000, v49
	v_rcp_f32_e32 v138, v48
	v_pk_mov_b32 v[48:49], v[82:83], v[52:53] op_sel:[1,0]
	v_add_f32_e32 v137, v119, v76
	v_pk_mul_f32 v[118:119], v[4:5], v[48:49]
	v_fma_f32 v68, v14, v68, v26
	v_add_f32_e32 v76, v120, v118
	v_add_f32_e32 v120, v76, v119
	v_mul_f32_e32 v76, 0xbfb8aa3b, v120
	v_exp_f32_e32 v118, v76
	v_cvt_pk_bf16_f32 v76, v129, v136
	v_add_f32_e32 v129, v137, v77
	v_mul_f32_e32 v77, v135, v138
	v_add_f32_e32 v118, 1.0, v118
	v_rcp_f32_e32 v135, v118
	v_pk_mul_f32 v[118:119], v[94:95], v[72:73]
	v_pk_mul_f32 v[48:49], v[12:13], v[48:49]
	v_add_f32_e32 v118, v121, v118
	v_add_f32_e32 v121, v118, v119
	v_pk_mul_f32 v[118:119], v[4:5], v[52:53]
	v_mul_f32_e32 v120, v120, v135
	v_add_f32_e32 v118, v122, v118
	v_mul_f32_e32 v122, 0xbfb8aa3b, v123
	v_cvt_pk_bf16_f32 v77, v77, v120
	global_store_dwordx4 v[84:85], v[74:77], off nt
	v_mul_f32_e32 v84, 0xbfb8aa3b, v128
	v_exp_f32_e32 v122, v122
	v_add_f32_e32 v74, v118, v119
	v_mul_f32_e32 v76, 0xbfb8aa3b, v124
	v_mul_f32_e32 v77, 0xbfb8aa3b, v125
	v_exp_f32_e32 v84, v84
	v_mul_f32_e32 v85, 0xbfb8aa3b, v134
	v_mul_f32_e32 v120, 0xbfb8aa3b, v74
	v_exp_f32_e32 v76, v76
	v_exp_f32_e32 v77, v77
	v_exp_f32_e32 v85, v85
	v_mul_f32_e32 v118, 0xbfb8aa3b, v129
	v_exp_f32_e32 v120, v120
	v_exp_f32_e32 v118, v118
	v_mul_f32_e32 v119, 0xbfb8aa3b, v121
	v_add_f32_e32 v75, 1.0, v122
	v_add_f32_e32 v84, 1.0, v84
	v_exp_f32_e32 v119, v119
	v_rcp_f32_e32 v75, v75
	v_add_f32_e32 v76, 1.0, v76
	v_add_f32_e32 v77, 1.0, v77
	v_rcp_f32_e32 v84, v84
	v_add_f32_e32 v85, 1.0, v85
	v_add_f32_e32 v120, 1.0, v120
	v_rcp_f32_e32 v76, v76
	v_rcp_f32_e32 v77, v77
	v_rcp_f32_e32 v85, v85
	v_add_f32_e32 v118, 1.0, v118
	v_rcp_f32_e32 v120, v120
	v_rcp_f32_e32 v118, v118
	v_add_f32_e32 v119, 1.0, v119
	v_mul_f32_e32 v75, v123, v75
	v_mul_f32_e32 v84, v128, v84
	v_rcp_f32_e32 v119, v119
	v_mul_f32_e32 v76, v124, v76
	v_mul_f32_e32 v77, v125, v77
	v_mul_f32_e32 v85, v134, v85
	v_mul_f32_e32 v120, v74, v120
	v_cvt_pk_bf16_f32 v74, v75, v76
	v_cvt_pk_bf16_f32 v75, v77, v84
	v_or_b32_e32 v84, 12, v131
	v_mul_f32_e32 v118, v129, v118
	v_cvt_pk_bf16_f32 v76, v85, v118
	v_mad_i64_i32 v[84:85], s[6:7], v84, s35, v[96:97]
	v_lshl_add_u64 v[84:85], v[84:85], 0, v[110:111]
	v_mul_f32_e32 v119, v121, v119
	v_cvt_pk_bf16_f32 v77, v119, v120
	global_store_dwordx4 v[84:85], v[74:77], off nt
	v_fma_f32 v59, v21, v59, v33
	v_fmac_f32_e32 v33, v21, v50
	v_pk_mul_f32 v[74:75], v[126:127], v[86:87]
	v_fma_f32 v77, v16, v80, v28
	v_add_f32_e32 v62, v62, v74
	v_add_f32_e32 v80, v62, v75
	v_pk_mul_f32 v[74:75], v[22:23], v[88:89]
	v_fma_f32 v76, v15, v78, v27
	v_add_f32_e32 v62, v64, v74
	v_fma_f32 v78, v17, v82, v29
	v_add_f32_e32 v82, v62, v75
	v_pk_mul_f32 v[74:75], v[106:107], v[90:91]
	v_add_f32_e32 v48, v78, v48
	v_add_f32_e32 v62, v66, v74
	v_add_f32_e32 v84, v62, v75
	v_pk_mul_f32 v[74:75], v[24:25], v[92:93]
	v_fma_f32 v62, v19, v65, v31
	v_add_f32_e32 v58, v58, v74
	v_add_f32_e32 v85, v58, v75
	v_pk_mul_f32 v[74:75], v[108:109], v[112:113]
	v_add_f32_e32 v112, v48, v49
	v_add_f32_e32 v58, v68, v74
	v_add_f32_e32 v86, v58, v75
	v_pk_mul_f32 v[74:75], v[10:11], v[114:115]
	v_or_b32_e32 v48, 13, v131
	v_add_f32_e32 v58, v76, v74
	v_add_f32_e32 v88, v58, v75
	v_pk_mul_f32 v[74:75], v[102:103], v[116:117]
	v_mad_i64_i32 v[48:49], s[6:7], v48, s35, v[96:97]
	v_add_f32_e32 v58, v77, v74
	v_add_f32_e32 v92, v58, v75
	v_lshl_add_u64 v[74:75], v[48:49], 0, v[110:111]
	v_fma_f32 v58, v18, v63, v30
	v_pk_mul_f32 v[48:49], v[126:127], v[54:55]
	v_fma_f32 v63, v20, v67, v32
	v_add_f32_e32 v48, v58, v48
	v_add_f32_e32 v77, v48, v49
	v_pk_mul_f32 v[48:49], v[22:23], v[56:57]
	v_fma_f32 v66, v16, v81, v28
	v_add_f32_e32 v48, v62, v48
	v_add_f32_e32 v81, v48, v49
	v_pk_mul_f32 v[48:49], v[106:107], v[60:61]
	v_fma_f32 v76, v17, v83, v29
	v_add_f32_e32 v48, v63, v48
	v_add_f32_e32 v83, v48, v49
	v_pk_mul_f32 v[48:49], v[24:25], v[50:51]
	v_fma_f32 v64, v14, v69, v26
	v_add_f32_e32 v48, v59, v48
	v_add_f32_e32 v87, v48, v49
	v_pk_mul_f32 v[48:49], v[108:109], v[46:47]
	v_fma_f32 v65, v15, v79, v27
	v_add_f32_e32 v48, v64, v48
	v_add_f32_e32 v89, v48, v49
	v_pk_mul_f32 v[48:49], v[10:11], v[70:71]
	v_pk_mul_f32 v[58:59], v[102:103], v[72:73]
	v_add_f32_e32 v48, v65, v48
	v_add_f32_e32 v93, v48, v49
	v_lshlrev_b32_e32 v49, 16, v42
	v_lshlrev_b32_e32 v48, 16, v38
	v_pk_mov_b32 v[62:63], v[54:55], v[48:49] op_sel:[1,0]
	v_add_f32_e32 v58, v66, v58
	v_pk_mul_f32 v[64:65], v[104:105], v[62:63]
	v_add_f32_e32 v113, v58, v59
	v_add_f32_e32 v55, v80, v64
	v_add_f32_e32 v55, v55, v65
	v_mul_f32_e32 v64, 0xbfb8aa3b, v55
	v_exp_f32_e32 v67, v64
	v_and_b32_e32 v59, 0xffff0000, v42
	v_pk_mul_f32 v[64:65], v[12:13], v[52:53]
	v_lshlrev_b32_e32 v80, 16, v40
	v_add_f32_e32 v58, 1.0, v67
	v_rcp_f32_e32 v78, v58
	v_and_b32_e32 v58, 0xffff0000, v38
	v_pk_mov_b32 v[66:67], v[56:57], v[58:59] op_sel:[1,0]
	v_add_f32_e32 v57, v76, v64
	v_pk_mul_f32 v[68:69], v[6:7], v[66:67]
	v_add_f32_e32 v57, v57, v65
	v_add_f32_e32 v38, v82, v68
	v_add_f32_e32 v38, v38, v69
	v_mul_f32_e32 v42, 0xbfb8aa3b, v38
	v_exp_f32_e32 v42, v42
	v_pk_mul_f32 v[64:65], v[104:105], v[48:49]
	v_lshlrev_b32_e32 v68, 16, v39
	v_lshlrev_b32_e32 v69, 16, v43
	v_add_f32_e32 v42, 1.0, v42
	v_rcp_f32_e32 v42, v42
	v_add_f32_e32 v48, v77, v64
	v_pk_mov_b32 v[76:77], v[60:61], v[68:69] op_sel:[1,0]
	v_mul_f32_e32 v55, v55, v78
	v_pk_mul_f32 v[78:79], v[98:99], v[76:77]
	v_mul_f32_e32 v38, v38, v42
	v_add_f32_e32 v42, v84, v78
	v_add_f32_e32 v48, v48, v65
	v_pk_mul_f32 v[64:65], v[6:7], v[58:59]
	v_add_f32_e32 v58, v42, v79
	v_mul_f32_e32 v42, 0xbfb8aa3b, v58
	v_exp_f32_e32 v42, v42
	v_add_f32_e32 v61, v81, v64
	v_cvt_pk_bf16_f32 v38, v55, v38
	v_add_f32_e32 v55, v61, v65
	v_add_f32_e32 v42, 1.0, v42
	v_rcp_f32_e32 v61, v42
	v_and_b32_e32 v43, 0xffff0000, v43
	v_and_b32_e32 v42, 0xffff0000, v39
	v_pk_mov_b32 v[64:65], v[50:51], v[42:43] op_sel:[1,0]
	v_lshlrev_b32_e32 v81, 16, v44
	v_pk_mul_f32 v[78:79], v[8:9], v[64:65]
	v_mul_f32_e32 v58, v58, v61
	v_add_f32_e32 v39, v85, v78
	v_add_f32_e32 v39, v39, v79
	v_mul_f32_e32 v51, 0xbfb8aa3b, v39
	v_exp_f32_e32 v51, v51
	v_pk_mul_f32 v[78:79], v[98:99], v[68:69]
	v_fma_f32 v18, v18, v54, v30
	v_add_f32_e32 v61, v83, v78
	v_add_f32_e32 v51, 1.0, v51
	v_rcp_f32_e32 v51, v51
	v_pk_mov_b32 v[82:83], v[46:47], v[80:81] op_sel:[1,0]
	v_add_f32_e32 v61, v61, v79
	v_pk_mul_f32 v[84:85], v[100:101], v[82:83]
	v_pk_mul_f32 v[78:79], v[8:9], v[42:43]
	v_add_f32_e32 v47, v86, v84
	v_add_f32_e32 v47, v47, v85
	v_mul_f32_e32 v39, v39, v51
	v_add_f32_e32 v51, v87, v78
	v_mul_f32_e32 v68, 0xbfb8aa3b, v47
	v_add_f32_e32 v51, v51, v79
	v_and_b32_e32 v79, 0xffff0000, v44
	v_and_b32_e32 v78, 0xffff0000, v40
	v_exp_f32_e32 v68, v68
	v_pk_mov_b32 v[84:85], v[70:71], v[78:79] op_sel:[1,0]
	v_fma_f32 v21, v14, v46, v26
	v_pk_mul_f32 v[86:87], v[2:3], v[84:85]
	v_add_f32_e32 v42, 1.0, v68
	v_add_f32_e32 v40, v88, v86
	v_add_f32_e32 v40, v40, v87
	v_mul_f32_e32 v44, 0xbfb8aa3b, v40
	v_fma_f32 v26, v15, v70, v27
	v_pk_mul_f32 v[14:15], v[126:127], v[62:63]
	v_rcp_f32_e32 v42, v42
	v_exp_f32_e32 v44, v44
	v_add_f32_e32 v14, v18, v14
	v_fma_f32 v19, v19, v56, v31
	v_fmac_f32_e32 v29, v17, v52
	v_add_f32_e32 v17, v14, v15
	v_pk_mul_f32 v[14:15], v[22:23], v[66:67]
	v_pk_mul_f32 v[86:87], v[100:101], v[80:81]
	v_add_f32_e32 v14, v19, v14
	v_fma_f32 v20, v20, v60, v32
	v_add_f32_e32 v18, v14, v15
	v_pk_mul_f32 v[14:15], v[106:107], v[76:77]
	v_mul_f32_e32 v42, v47, v42
	v_add_f32_e32 v47, v89, v86
	v_add_f32_e32 v44, 1.0, v44
	v_add_f32_e32 v14, v20, v14
	v_add_f32_e32 v47, v47, v87
	v_rcp_f32_e32 v44, v44
	v_lshlrev_b32_e32 v86, 16, v41
	v_lshlrev_b32_e32 v87, 16, v45
	v_add_f32_e32 v19, v14, v15
	v_pk_mul_f32 v[14:15], v[24:25], v[64:65]
	v_pk_mov_b32 v[88:89], v[72:73], v[86:87] op_sel:[1,0]
	v_add_f32_e32 v14, v33, v14
	v_pk_mul_f32 v[90:91], v[94:95], v[88:89]
	v_add_f32_e32 v20, v14, v15
	v_pk_mul_f32 v[14:15], v[108:109], v[82:83]
	v_pk_mul_f32 v[10:11], v[10:11], v[84:85]
	v_cvt_pk_bf16_f32 v39, v58, v39
	v_add_f32_e32 v58, v92, v90
	v_add_f32_e32 v14, v21, v14
	v_add_f32_e32 v10, v26, v10
	v_add_f32_e32 v58, v58, v91
	v_mul_f32_e32 v71, v40, v44
	v_pk_mul_f32 v[90:91], v[2:3], v[78:79]
	v_and_b32_e32 v45, 0xffff0000, v45
	v_and_b32_e32 v44, 0xffff0000, v41
	v_fma_f32 v16, v16, v72, v28
	v_add_f32_e32 v14, v14, v15
	v_add_f32_e32 v15, v10, v11
	v_pk_mul_f32 v[10:11], v[102:103], v[88:89]
	v_add_f32_e32 v73, v93, v90
	v_pk_mov_b32 v[92:93], v[52:53], v[44:45] op_sel:[1,0]
	v_add_f32_e32 v10, v16, v10
	v_add_f32_e32 v16, v10, v11
	v_pk_mul_f32 v[10:11], v[12:13], v[92:93]
	v_mul_f32_e32 v68, 0xbfb8aa3b, v58
	v_add_f32_e32 v10, v29, v10
	v_add_f32_e32 v12, v10, v11
	v_lshlrev_b32_e32 v11, 16, v34
	v_mov_b32_e32 v10, v49
	v_pk_mul_f32 v[10:11], v[104:105], v[10:11]
	v_exp_f32_e32 v68, v68
	v_add_f32_e32 v10, v17, v10
	v_add_f32_e32 v13, v10, v11
	v_and_b32_e32 v11, 0xffff0000, v34
	v_mov_b32_e32 v10, v59
	v_pk_mul_f32 v[6:7], v[6:7], v[10:11]
	v_add_f32_e32 v40, 1.0, v68
	v_add_f32_e32 v6, v18, v6
	v_add_f32_e32 v10, v6, v7
	v_lshlrev_b32_e32 v7, 16, v35
	v_mov_b32_e32 v6, v69
	v_pk_mul_f32 v[6:7], v[98:99], v[6:7]
	v_rcp_f32_e32 v68, v40
	v_add_f32_e32 v6, v19, v6
	v_add_f32_e32 v11, v6, v7
	v_and_b32_e32 v7, 0xffff0000, v35
	v_mov_b32_e32 v6, v43
	v_pk_mul_f32 v[40:41], v[4:5], v[92:93]
	v_pk_mul_f32 v[6:7], v[8:9], v[6:7]
	v_add_f32_e32 v40, v112, v40
	v_add_f32_e32 v6, v20, v6
	v_add_f32_e32 v41, v40, v41
	v_add_f32_e32 v8, v6, v7
	v_lshlrev_b32_e32 v7, 16, v36
	v_mov_b32_e32 v6, v81
	v_mul_f32_e32 v40, 0xbfb8aa3b, v41
	v_pk_mul_f32 v[6:7], v[100:101], v[6:7]
	v_exp_f32_e32 v53, v40
	v_add_f32_e32 v6, v14, v6
	v_add_f32_e32 v9, v6, v7
	v_and_b32_e32 v7, 0xffff0000, v36
	v_mov_b32_e32 v6, v79
	v_pk_mul_f32 v[2:3], v[2:3], v[6:7]
	v_add_f32_e32 v53, 1.0, v53
	v_add_f32_e32 v2, v15, v2
	v_add_f32_e32 v6, v2, v3
	v_lshlrev_b32_e32 v3, 16, v37
	v_mov_b32_e32 v2, v87
	v_rcp_f32_e32 v53, v53
	v_pk_mul_f32 v[2:3], v[94:95], v[2:3]
	v_cvt_pk_bf16_f32 v40, v42, v71
	v_add_f32_e32 v42, v73, v91
	v_pk_mul_f32 v[90:91], v[94:95], v[86:87]
	v_add_f32_e32 v2, v16, v2
	v_mul_f32_e32 v58, v58, v68
	v_add_f32_e32 v68, v113, v90
	v_add_f32_e32 v7, v2, v3
	v_and_b32_e32 v3, 0xffff0000, v37
	v_mov_b32_e32 v2, v45
	v_add_f32_e32 v68, v68, v91
	v_pk_mul_f32 v[90:91], v[4:5], v[44:45]
	v_pk_mul_f32 v[2:3], v[4:5], v[2:3]
	v_mul_f32_e32 v4, 0xbfb8aa3b, v10
	v_mul_f32_e32 v5, 0xbfb8aa3b, v11
	v_mul_f32_e32 v41, v41, v53
	v_exp_f32_e32 v4, v4
	v_exp_f32_e32 v5, v5
	v_mul_f32_e32 v53, 0xbfb8aa3b, v48
	v_cvt_pk_bf16_f32 v41, v58, v41
	global_store_dwordx4 v[74:75], v[38:41], off nt
	v_exp_f32_e32 v53, v53
	v_add_f32_e32 v44, v57, v90
	v_mul_f32_e32 v40, 0xbfb8aa3b, v55
	v_exp_f32_e32 v40, v40
	v_add_f32_e32 v38, v44, v91
	v_mul_f32_e32 v44, 0xbfb8aa3b, v51
	v_mul_f32_e32 v14, 0xbfb8aa3b, v13
	v_add_f32_e32 v2, v12, v2
	v_add_f32_e32 v4, 1.0, v4
	v_add_f32_e32 v5, 1.0, v5
	v_mul_f32_e32 v12, 0xbfb8aa3b, v8
	v_exp_f32_e32 v44, v44
	v_exp_f32_e32 v14, v14
	v_rcp_f32_e32 v4, v4
	v_rcp_f32_e32 v5, v5
	v_exp_f32_e32 v12, v12
	v_add_f32_e32 v39, 1.0, v53
	v_add_f32_e32 v40, 1.0, v40
	v_rcp_f32_e32 v39, v39
	v_rcp_f32_e32 v40, v40
	v_add_f32_e32 v44, 1.0, v44
	v_mul_f32_e32 v53, 0xbfb8aa3b, v42
	v_add_f32_e32 v2, v2, v3
	v_add_f32_e32 v3, 1.0, v14
	v_mul_f32_e32 v4, v10, v4
	v_mul_f32_e32 v5, v11, v5
	v_add_f32_e32 v10, 1.0, v12
	v_mul_f32_e32 v11, 0xbfb8aa3b, v9
	v_mul_f32_e32 v12, 0xbfb8aa3b, v6
	v_rcp_f32_e32 v44, v44
	v_exp_f32_e32 v53, v53
	v_rcp_f32_e32 v3, v3
	v_rcp_f32_e32 v10, v10
	v_exp_f32_e32 v11, v11
	v_exp_f32_e32 v12, v12
	v_mul_f32_e32 v41, 0xbfb8aa3b, v61
	v_mul_f32_e32 v39, v48, v39
	v_mul_f32_e32 v40, v55, v40
	v_mul_f32_e32 v48, 0xbfb8aa3b, v47
	v_mul_f32_e32 v55, 0xbfb8aa3b, v38
	v_exp_f32_e32 v41, v41
	v_exp_f32_e32 v48, v48
	v_exp_f32_e32 v55, v55
	v_mul_f32_e32 v44, v51, v44
	v_add_f32_e32 v51, 1.0, v53
	v_mul_f32_e32 v53, 0xbfb8aa3b, v68
	v_mul_f32_e32 v3, v13, v3
	v_mul_f32_e32 v8, v8, v10
	v_add_f32_e32 v10, 1.0, v11
	v_add_f32_e32 v11, 1.0, v12
	v_mul_f32_e32 v12, 0xbfb8aa3b, v7
	v_mul_f32_e32 v13, 0xbfb8aa3b, v2
	v_exp_f32_e32 v53, v53
	v_exp_f32_e32 v12, v12
	v_exp_f32_e32 v13, v13
	v_add_f32_e32 v41, 1.0, v41
	v_add_f32_e32 v48, 1.0, v48
	v_rcp_f32_e32 v51, v51
	v_add_f32_e32 v55, 1.0, v55
	v_rcp_f32_e32 v41, v41
	v_rcp_f32_e32 v48, v48
	v_rcp_f32_e32 v55, v55
	v_add_f32_e32 v53, 1.0, v53
	v_rcp_f32_e32 v11, v11
	v_add_f32_e32 v12, 1.0, v12
	v_add_f32_e32 v13, 1.0, v13
	v_rcp_f32_e32 v53, v53
	v_mul_f32_e32 v42, v42, v51
	v_rcp_f32_e32 v10, v10
	v_rcp_f32_e32 v12, v12
	v_rcp_f32_e32 v13, v13
	v_mul_f32_e32 v41, v61, v41
	v_mul_f32_e32 v47, v47, v48
	v_mul_f32_e32 v51, v38, v55
	v_cvt_pk_bf16_f32 v38, v39, v40
	v_cvt_pk_bf16_f32 v39, v41, v44
	v_cvt_pk_bf16_f32 v40, v47, v42
	v_or_b32_e32 v42, 14, v131
	v_mad_i64_i32 v[74:75], s[6:7], v42, s35, v[96:97]
	v_lshl_add_u64 v[74:75], v[74:75], 0, v[110:111]
	v_mul_f32_e32 v6, v6, v11
	v_mul_f32_e32 v48, v68, v53
	v_cvt_pk_bf16_f32 v41, v48, v51
	global_store_dwordx4 v[74:75], v[38:41], off nt
	v_mul_f32_e32 v9, v9, v10
	v_mul_f32_e32 v7, v7, v12
	v_mul_f32_e32 v10, v2, v13
	v_cvt_pk_bf16_f32 v2, v3, v4
	v_cvt_pk_bf16_f32 v3, v5, v8
	v_cvt_pk_bf16_f32 v4, v9, v6
	v_or_b32_e32 v6, 15, v131
	v_cvt_pk_bf16_f32 v5, v7, v10
	v_mad_i64_i32 v[6:7], s[6:7], v6, s35, v[96:97]
	v_lshl_add_u64 v[6:7], v[6:7], 0, v[110:111]
	global_store_dwordx4 v[6:7], v[2:5], off nt
	s_andn2_b64 exec, exec, s[16:17]
	s_cbranch_execz .LBB0_305
